# C1 with code placement restored: one s_nop after each edit site so every unchanged block sits at a byte shift of 0 mod 8 from its baseline address
# baseline (speedup 1.0000x reference)
.LBB0_125:
	s_ashr_i32 s46, s10, 2
	s_ashr_i32 s47, s46, 31
	v_cvt_f32_i32_e32 v204, v86
	v_cvt_f32_i32_e32 v86, v58
	v_cvt_f32_i32_e32 v58, v6
	v_mov_b32_e32 v6, 0
	s_lshl_b64 s[48:49], s[46:47], 26
	s_and_b32 s31, s10, 3
	s_lshl_b32 s35, s44, 8
	v_cvt_f32_i32_e32 v170, v104
	v_cvt_f32_i32_e32 v104, v52
	v_cvt_f32_i32_e32 v171, v105
	v_add3_u32 v52, s35, v159, v6
	s_add_u32 s35, s40, s48
	v_cvt_f32_i32_e32 v162, v70
	v_cvt_f32_i32_e32 v105, v53
	v_cvt_f32_i32_e32 v70, v42
	v_mov_b32_e32 v42, 0
	v_ashrrev_i32_e32 v53, 31, v52
	s_addc_u32 s45, s41, s49
	s_lshl_b32 s10, s10, 8
	v_cvt_f32_i32_e32 v205, v87
	v_cvt_f32_i32_e32 v210, v88
	v_cvt_f32_i32_e32 v88, v62
	v_cvt_f32_i32_e32 v87, v59
	v_cvt_f32_i32_e32 v62, v50
	v_cvt_f32_i32_e32 v59, v7
	v_lshl_add_u64 v[6:7], v[52:53], 2, s[14:15]
	v_add_lshl_u32 v50, v42, v1, 3
	s_or_b32 s47, s10, s60
	s_lshl_b64 s[48:49], s[10:11], 2
	s_add_u32 s48, s64, s48
	s_addc_u32 s49, s65, s49
	v_ashrrev_i32_e32 v253, 31, v50
	v_mov_b32_e32 v252, v50
	v_lshl_add_u64 v[252:253], v[252:253], 2, s[48:49]
	global_load_dwordx4 v[236:239], v[252:253], off
	global_load_dwordx4 v[240:243], v[252:253], off offset:16
	global_load_dwordx4 v[244:247], v[252:253], off offset:512
	global_load_dwordx4 v[248:251], v[252:253], off offset:528
	s_nop 0
	v_cvt_f32_i32_e32 v150, v64
	v_cvt_f32_i32_e32 v64, v54
	global_load_dword v54, v[6:7], off
	v_add_u32_e32 v6, s47, v50
	v_ashrrev_i32_e32 v7, 31, v6
	v_cvt_f32_i32_e32 v154, v112
	v_cvt_f32_i32_e32 v112, v90
	v_cvt_f32_i32_e32 v189, v77
	v_cvt_f32_i32_e32 v188, v76
	v_cvt_f32_i32_e32 v77, v47
	v_cvt_f32_i32_e32 v76, v46
	v_lshl_add_u64 v[46:47], v[6:7], 2, s[16:17]
	v_cvt_f32_i32_e32 v90, v2
	v_add_u32_e32 v2, 0x80, v6
	v_cvt_f32_i32_e32 v155, v113
	v_cvt_f32_i32_e32 v113, v91
	v_cvt_f32_i32_e32 v187, v79
	v_cvt_f32_i32_e32 v186, v78
	v_cvt_f32_i32_e32 v195, v81
	v_cvt_f32_i32_e32 v194, v80
	v_cvt_f32_i32_e32 v163, v71
	v_cvt_f32_i32_e32 v81, v49
	v_cvt_f32_i32_e32 v80, v48
	v_cvt_f32_i32_e32 v71, v43
	v_cvt_f32_i32_e32 v79, v45
	v_cvt_f32_i32_e32 v78, v44
	global_load_dwordx4 v[42:45], v[46:47], off offset:16
	s_nop 0
	global_load_dwordx4 v[46:49], v[46:47], off
	v_cvt_f32_i32_e32 v91, v3
	v_ashrrev_i32_e32 v3, 31, v2
	v_cvt_f32_i32_e32 v196, v40
	v_lshl_add_u64 v[6:7], v[2:3], 2, s[16:17]
	v_cvt_f32_i32_e32 v40, v30
	v_add_u32_e32 v30, 16, v52
	v_cvt_f32_i32_e32 v209, v117
	v_cvt_f32_i32_e32 v208, v116
	v_cvt_f32_i32_e32 v221, v97
	v_cvt_f32_i32_e32 v220, v96
	v_cvt_f32_i32_e32 v117, v93
	v_cvt_f32_i32_e32 v116, v92
	v_cvt_f32_i32_e32 v97, v9
	v_cvt_f32_i32_e32 v96, v8
	v_cvt_f32_i32_e32 v93, v5
	v_cvt_f32_i32_e32 v92, v4
	v_cvt_f32_i32_e32 v197, v41
	v_cvt_f32_i32_e32 v41, v31
	global_load_dwordx4 v[2:5], v[6:7], off offset:16
	s_nop 0
	global_load_dwordx4 v[6:9], v[6:7], off
	v_ashrrev_i32_e32 v31, 31, v30
	v_cvt_f32_i32_e32 v173, v11
	v_cvt_f32_i32_e32 v172, v10
	v_lshl_add_u64 v[10:11], v[30:31], 2, s[14:15]
	v_cvt_f32_i32_e32 v160, v66
	global_load_dword v66, v[10:11], off
	v_cvt_f32_i32_e32 v206, v118
	v_cvt_f32_i32_e32 v118, v18
	v_add_u32_e32 v18, 32, v52
	v_cvt_f32_i32_e32 v207, v119
	v_cvt_f32_i32_e32 v119, v19
	v_ashrrev_i32_e32 v19, 31, v18
	v_lshl_add_u64 v[10:11], v[18:19], 2, s[14:15]
	v_cvt_f32_i32_e32 v156, v110
	v_cvt_f32_i32_e32 v110, v98
	v_cvt_f32_i32_e32 v98, v22
	global_load_dword v22, v[10:11], off
	v_cvt_f32_i32_e32 v218, v94
	v_cvt_f32_i32_e32 v94, v26
	v_add_u32_e32 v26, 48, v52
	v_cvt_f32_i32_e32 v222, v124
	v_cvt_f32_i32_e32 v219, v95
	v_cvt_f32_i32_e32 v95, v27
	v_ashrrev_i32_e32 v27, 31, v26
	v_add_u32_e32 v216, 0x80, v52
	v_add_u32_e32 v200, 0x90, v52
	v_add_u32_e32 v180, 0xa0, v52
	v_add_u32_e32 v124, 0xb0, v52
	v_cvt_f32_i32_e32 v223, v125
	v_lshl_add_u64 v[10:11], v[26:27], 2, s[14:15]
	v_ashrrev_i32_e32 v217, 31, v216
	v_ashrrev_i32_e32 v201, 31, v200
	v_ashrrev_i32_e32 v181, 31, v180
	v_ashrrev_i32_e32 v125, 31, v124
	v_cvt_f32_i32_e32 v225, v127
	v_cvt_f32_i32_e32 v224, v126
	v_cvt_f32_i32_e32 v153, v123
	v_cvt_f32_i32_e32 v152, v122
	v_cvt_f32_i32_e32 v213, v121
	v_cvt_f32_i32_e32 v212, v120
	v_cvt_f32_i32_e32 v202, v114
	v_cvt_f32_i32_e32 v166, v100
	v_cvt_f32_i32_e32 v177, v13
	v_cvt_f32_i32_e32 v176, v12
	v_cvt_f32_i32_e32 v121, v15
	v_cvt_f32_i32_e32 v120, v14
	v_cvt_f32_i32_e32 v127, v17
	v_cvt_f32_i32_e32 v126, v16
	v_cvt_f32_i32_e32 v123, v21
	v_cvt_f32_i32_e32 v122, v20
	v_cvt_f32_i32_e32 v100, v28
	v_lshl_add_u64 v[12:13], v[216:217], 2, s[14:15]
	v_lshl_add_u64 v[14:15], v[200:201], 2, s[14:15]
	v_lshl_add_u64 v[16:17], v[180:181], 2, s[14:15]
	v_lshl_add_u64 v[20:21], v[124:125], 2, s[14:15]
	global_load_dword v28, v[10:11], off
	global_load_dword v214, v[12:13], off
	global_load_dword v190, v[14:15], off
	global_load_dword v158, v[16:17], off
	global_load_dword v114, v[20:21], off
	v_cvt_f32_i32_e32 v227, v129
	v_cvt_f32_i32_e32 v226, v128
	s_lshl_b32 s47, s31, 9
	s_add_u32 s48, s35, s47
	v_cvt_f32_i32_e32 v183, v75
	v_cvt_f32_i32_e32 v182, v74
	v_cvt_f32_i32_e32 v169, v73
	v_cvt_f32_i32_e32 v168, v72
	v_cvt_f32_i32_e32 v179, v37
	v_cvt_f32_i32_e32 v178, v36
	s_addc_u32 s49, s45, 0
	v_add_u32_e32 v14, s60, v50
	v_lshlrev_b64 v[10:11], 11, v[52:53]
	s_waitcnt vmcnt(0)
	v_pk_mul_f32 v[72:73], v[54:55], v[226:227] op_sel_hi:[0,1]
	v_pk_mul_f32 v[74:75], v[54:55], v[224:225] op_sel_hi:[0,1]
	v_pk_mul_f32 v[36:37], v[54:55], v[152:153] op_sel_hi:[0,1]
	v_cvt_f32_i32_e32 v193, v109
	v_cvt_f32_i32_e32 v192, v108
	v_cvt_f32_i32_e32 v109, v103
	v_cvt_f32_i32_e32 v108, v102
	v_cvt_f32_i32_e32 v175, v35
	v_cvt_f32_i32_e32 v174, v34
	v_cvt_f32_i32_e32 v103, v25
	v_cvt_f32_i32_e32 v102, v24
	v_lshl_add_u64 v[16:17], s[48:49], 0, v[10:11]
	v_pk_mul_f32 v[12:13], v[72:73], v[48:49]
	v_pk_mul_f32 v[10:11], v[74:75], v[46:47]
	v_pk_mul_f32 v[34:35], v[54:55], v[222:223] op_sel_hi:[0,1]
	v_pk_mul_f32 v[24:25], v[36:37], v[42:43]
	v_ashrrev_i32_e32 v15, 31, v14
	v_cvt_f32_i32_e32 v203, v115
	v_pk_mul_f32 v[20:21], v[34:35], v[44:45]
	v_cvt_pk_bf16_f32 v10, v10, v11
	v_cvt_pk_bf16_f32 v11, v12, v13
	v_cvt_pk_bf16_f32 v12, v24, v25
	v_lshlrev_b64 v[152:153], 1, v[14:15]
	v_pk_mul_f32 v[24:25], v[54:55], v[218:219] op_sel_hi:[0,1]
	v_cvt_f32_i32_e32 v211, v89
	v_cvt_f32_i32_e32 v199, v33
	v_cvt_f32_i32_e32 v198, v32
	v_cvt_pk_bf16_f32 v13, v20, v21
	v_lshl_add_u64 v[32:33], v[16:17], 0, v[152:153]
	v_pk_mul_f32 v[20:21], v[54:55], v[220:221] op_sel_hi:[0,1]
	v_pk_mul_f32 v[14:15], v[24:25], v[6:7]
	v_cvt_f32_i32_e32 v83, v83
	v_cvt_f32_i32_e32 v82, v82
	v_cvt_f32_i32_e32 v85, v85
	v_cvt_f32_i32_e32 v84, v84
	global_store_dwordx4 v[32:33], v[10:13], off
	v_pk_mul_f32 v[16:17], v[20:21], v[8:9]
	v_cvt_pk_bf16_f32 v14, v14, v15
	v_cvt_f32_i32_e32 v157, v111
	v_pk_mul_f32 v[10:11], v[54:55], v[116:117] op_sel_hi:[0,1]
	v_pk_mul_f32 v[12:13], v[54:55], v[112:113] op_sel_hi:[0,1]
	v_cvt_pk_bf16_f32 v15, v16, v17
	v_cvt_f32_i32_e32 v185, v107
	v_cvt_f32_i32_e32 v184, v106
	v_cvt_f32_i32_e32 v151, v65
	v_cvt_f32_i32_e32 v65, v55
	v_cvt_f32_i32_e32 v107, v57
	v_cvt_f32_i32_e32 v106, v56
	v_pk_mul_f32 v[52:53], v[10:11], v[4:5]
	v_pk_mul_f32 v[54:55], v[12:13], v[2:3]
	v_pk_mul_f32 v[112:113], v[66:67], v[212:213] op_sel_hi:[0,1]
	v_cvt_pk_bf16_f32 v16, v54, v55
	v_cvt_pk_bf16_f32 v17, v52, v53
	global_store_dwordx4 v[32:33], v[14:17], off offset:256
	v_pk_mul_f32 v[116:117], v[66:67], v[206:207] op_sel_hi:[0,1]
	v_pk_mul_f32 v[56:57], v[66:67], v[208:209] op_sel_hi:[0,1]
	v_lshlrev_b64 v[14:15], 11, v[30:31]
	v_cvt_f32_i32_e32 v129, v61
	v_cvt_f32_i32_e32 v128, v60
	v_lshl_add_u64 v[30:31], s[48:49], 0, v[14:15]
	v_pk_mul_f32 v[16:17], v[112:113], v[48:49]
	v_pk_mul_f32 v[14:15], v[116:117], v[46:47]
	v_pk_mul_f32 v[60:61], v[66:67], v[202:203] op_sel_hi:[0,1]
	v_pk_mul_f32 v[32:33], v[56:57], v[44:45]
	v_cvt_f32_i32_e32 v165, v69
	v_cvt_f32_i32_e32 v164, v68
	v_pk_mul_f32 v[52:53], v[60:61], v[42:43]
	v_cvt_pk_bf16_f32 v14, v14, v15
	v_cvt_pk_bf16_f32 v15, v16, v17
	v_lshl_add_u64 v[68:69], v[30:31], 0, v[152:153]
	v_cvt_pk_bf16_f32 v16, v52, v53
	v_cvt_pk_bf16_f32 v17, v32, v33
	v_pk_mul_f32 v[30:31], v[66:67], v[210:211] op_sel_hi:[0,1]
	v_pk_mul_f32 v[32:33], v[66:67], v[204:205] op_sel_hi:[0,1]
	global_store_dwordx4 v[68:69], v[14:17], off
	v_pk_mul_f32 v[54:55], v[30:31], v[8:9]
	v_pk_mul_f32 v[52:53], v[32:33], v[6:7]
	v_pk_mul_f32 v[14:15], v[66:67], v[84:85] op_sel_hi:[0,1]
	v_pk_mul_f32 v[16:17], v[66:67], v[82:83] op_sel_hi:[0,1]
	v_cvt_f32_i32_e32 v161, v67
	v_pk_mul_f32 v[66:67], v[14:15], v[4:5]
	v_pk_mul_f32 v[82:83], v[16:17], v[2:3]
	v_cvt_pk_bf16_f32 v52, v52, v53
	v_cvt_pk_bf16_f32 v53, v54, v55
	v_lshlrev_b64 v[18:19], 11, v[18:19]
	v_cvt_pk_bf16_f32 v54, v82, v83
	v_cvt_pk_bf16_f32 v55, v66, v67
	v_pk_mul_f32 v[154:155], v[22:23], v[154:155] op_sel_hi:[0,1]
	v_pk_mul_f32 v[156:157], v[22:23], v[156:157] op_sel_hi:[0,1]
	v_cvt_f32_i32_e32 v167, v101
	global_store_dwordx4 v[68:69], v[52:55], off offset:256
	v_lshl_add_u64 v[18:19], s[48:49], 0, v[18:19]
	v_pk_mul_f32 v[82:83], v[22:23], v[192:193] op_sel_hi:[0,1]
	v_pk_mul_f32 v[54:55], v[154:155], v[48:49]
	v_pk_mul_f32 v[52:53], v[156:157], v[46:47]
	v_pk_mul_f32 v[84:85], v[22:23], v[184:185] op_sel_hi:[0,1]
	v_cvt_f32_i32_e32 v111, v99
	v_pk_mul_f32 v[66:67], v[82:83], v[44:45]
	v_pk_mul_f32 v[68:69], v[84:85], v[42:43]
	v_cvt_pk_bf16_f32 v52, v52, v53
	v_cvt_pk_bf16_f32 v53, v54, v55
	v_lshl_add_u64 v[184:185], v[18:19], 0, v[152:153]
	v_cvt_pk_bf16_f32 v54, v68, v69
	v_cvt_pk_bf16_f32 v55, v66, v67
	global_store_dwordx4 v[184:185], v[52:55], off
	v_pk_mul_f32 v[18:19], v[22:23], v[188:189] op_sel_hi:[0,1]
	v_cvt_f32_i32_e32 v99, v23
	v_pk_mul_f32 v[52:53], v[22:23], v[194:195] op_sel_hi:[0,1]
	v_pk_mul_f32 v[54:55], v[22:23], v[186:187] op_sel_hi:[0,1]
	v_pk_mul_f32 v[68:69], v[52:53], v[8:9]
	v_pk_mul_f32 v[66:67], v[54:55], v[6:7]
	v_pk_mul_f32 v[22:23], v[22:23], v[182:183] op_sel_hi:[0,1]
	v_pk_mul_f32 v[182:183], v[18:19], v[4:5]
	v_pk_mul_f32 v[186:187], v[22:23], v[2:3]
	v_cvt_pk_bf16_f32 v66, v66, v67
	v_cvt_pk_bf16_f32 v67, v68, v69
	v_lshlrev_b64 v[26:27], 11, v[26:27]
	v_cvt_pk_bf16_f32 v68, v186, v187
	v_cvt_pk_bf16_f32 v69, v182, v183
	v_pk_mul_f32 v[170:171], v[28:29], v[170:171] op_sel_hi:[0,1]
	v_pk_mul_f32 v[182:183], v[28:29], v[108:109] op_sel_hi:[0,1]
	v_pk_mul_f32 v[108:109], v[28:29], v[166:167] op_sel_hi:[0,1]
	global_store_dwordx4 v[184:185], v[66:69], off offset:256
	v_lshl_add_u64 v[26:27], s[48:49], 0, v[26:27]
	v_pk_mul_f32 v[110:111], v[28:29], v[110:111] op_sel_hi:[0,1]
	v_pk_mul_f32 v[68:69], v[170:171], v[48:49]
	v_pk_mul_f32 v[66:67], v[182:183], v[46:47]
	v_pk_mul_f32 v[166:167], v[108:109], v[44:45]
	v_cvt_f32_i32_e32 v89, v63
	v_pk_mul_f32 v[184:185], v[110:111], v[42:43]
	v_cvt_pk_bf16_f32 v66, v66, v67
	v_cvt_pk_bf16_f32 v67, v68, v69
	v_cvt_f32_i32_e32 v39, v39
	v_cvt_pk_bf16_f32 v68, v184, v185
	v_cvt_pk_bf16_f32 v69, v166, v167
	v_lshl_add_u64 v[166:167], v[26:27], 0, v[152:153]
	global_store_dwordx4 v[166:167], v[66:69], off
	v_cvt_f32_i32_e32 v38, v38
	v_cvt_f32_i32_e32 v101, v29
	v_pk_mul_f32 v[66:67], v[28:29], v[168:169] op_sel_hi:[0,1]
	v_pk_mul_f32 v[68:69], v[28:29], v[162:163] op_sel_hi:[0,1]
	v_pk_mul_f32 v[162:163], v[66:67], v[8:9]
	v_pk_mul_f32 v[168:169], v[68:69], v[6:7]
	v_pk_mul_f32 v[26:27], v[28:29], v[164:165] op_sel_hi:[0,1]
	v_pk_mul_f32 v[28:29], v[28:29], v[160:161] op_sel_hi:[0,1]
	v_cvt_pk_bf16_f32 v160, v168, v169
	v_cvt_pk_bf16_f32 v161, v162, v163
	v_pk_mul_f32 v[164:165], v[26:27], v[4:5]
	v_pk_mul_f32 v[184:185], v[28:29], v[2:3]
	v_pk_mul_f32 v[168:169], v[214:215], v[150:151] op_sel_hi:[0,1]
	v_cvt_pk_bf16_f32 v162, v184, v185
	v_cvt_pk_bf16_f32 v163, v164, v165
	global_store_dwordx4 v[166:167], v[160:163], off offset:256
	v_pk_mul_f32 v[128:129], v[214:215], v[128:129] op_sel_hi:[0,1]
	v_pk_mul_f32 v[184:185], v[214:215], v[88:89] op_sel_hi:[0,1]
	v_lshlrev_b64 v[160:161], 11, v[216:217]
	v_lshl_add_u64 v[160:161], s[48:49], 0, v[160:161]
	v_pk_mul_f32 v[88:89], v[48:49], v[168:169]
	v_pk_mul_f32 v[150:151], v[214:215], v[86:87] op_sel_hi:[0,1]
	v_pk_mul_f32 v[164:165], v[128:129], v[44:45]
	v_pk_mul_f32 v[162:163], v[46:47], v[184:185]
	v_pk_mul_f32 v[166:167], v[150:151], v[42:43]
	v_cvt_pk_bf16_f32 v86, v162, v163
	v_cvt_pk_bf16_f32 v87, v88, v89
	v_cvt_f32_i32_e32 v63, v51
	v_cvt_pk_bf16_f32 v88, v166, v167
	v_cvt_pk_bf16_f32 v89, v164, v165
	v_lshl_add_u64 v[164:165], v[160:161], 0, v[152:153]
	global_store_dwordx4 v[164:165], v[86:89], off
	v_pk_mul_f32 v[40:41], v[214:215], v[40:41] op_sel_hi:[0,1]
	v_pk_mul_f32 v[186:187], v[40:41], v[2:3]
	v_pk_mul_f32 v[88:89], v[214:215], v[38:39] op_sel_hi:[0,1]
	v_pk_mul_f32 v[86:87], v[214:215], v[196:197] op_sel_hi:[0,1]
	v_pk_mul_f32 v[160:161], v[88:89], v[6:7]
	v_pk_mul_f32 v[162:163], v[86:87], v[8:9]
	v_pk_mul_f32 v[38:39], v[214:215], v[198:199] op_sel_hi:[0,1]
	v_cvt_pk_bf16_f32 v160, v160, v161
	v_cvt_pk_bf16_f32 v161, v162, v163
	v_pk_mul_f32 v[166:167], v[38:39], v[4:5]
	v_cvt_pk_bf16_f32 v162, v186, v187
	v_pk_mul_f32 v[186:187], v[190:191], v[106:107] op_sel_hi:[0,1]
	v_cvt_pk_bf16_f32 v163, v166, v167
	global_store_dwordx4 v[164:165], v[160:163], off offset:256
	v_pk_mul_f32 v[188:189], v[190:191], v[64:65] op_sel_hi:[0,1]
	v_pk_mul_f32 v[64:65], v[48:49], v[186:187]
	v_lshlrev_b64 v[160:161], 11, v[200:201]
	v_lshl_add_u64 v[164:165], s[48:49], 0, v[160:161]
	v_pk_mul_f32 v[160:161], v[190:191], v[104:105] op_sel_hi:[0,1]
	v_pk_mul_f32 v[106:107], v[46:47], v[188:189]
	v_pk_mul_f32 v[162:163], v[190:191], v[62:63] op_sel_hi:[0,1]
	v_pk_mul_f32 v[104:105], v[44:45], v[160:161]
	v_pk_mul_f32 v[166:167], v[42:43], v[162:163]
	v_cvt_pk_bf16_f32 v62, v106, v107
	v_cvt_pk_bf16_f32 v63, v64, v65
	v_lshl_add_u64 v[192:193], v[164:165], 0, v[152:153]
	v_cvt_pk_bf16_f32 v64, v166, v167
	v_cvt_pk_bf16_f32 v65, v104, v105
	v_pk_mul_f32 v[104:105], v[190:191], v[178:179] op_sel_hi:[0,1]
	v_pk_mul_f32 v[106:107], v[190:191], v[174:175] op_sel_hi:[0,1]
	global_store_dwordx4 v[192:193], v[62:65], off
	v_pk_mul_f32 v[166:167], v[104:105], v[8:9]
	v_pk_mul_f32 v[164:165], v[106:107], v[6:7]
	v_pk_mul_f32 v[62:63], v[190:191], v[176:177] op_sel_hi:[0,1]
	v_pk_mul_f32 v[64:65], v[190:191], v[172:173] op_sel_hi:[0,1]
	v_pk_mul_f32 v[172:173], v[62:63], v[4:5]
	v_pk_mul_f32 v[174:175], v[64:65], v[2:3]
	v_cvt_pk_bf16_f32 v164, v164, v165
	v_cvt_pk_bf16_f32 v165, v166, v167
	v_pk_mul_f32 v[96:97], v[114:115], v[96:97] op_sel_hi:[0,1]
	v_cvt_pk_bf16_f32 v166, v174, v175
	v_cvt_pk_bf16_f32 v167, v172, v173
	global_store_dwordx4 v[192:193], v[164:167], off offset:256
	v_pk_mul_f32 v[174:175], v[158:159], v[76:77] op_sel_hi:[0,1]
	v_pk_mul_f32 v[172:173], v[158:159], v[80:81] op_sel_hi:[0,1]
	v_lshlrev_b64 v[164:165], 11, v[180:181]
	v_pk_mul_f32 v[166:167], v[158:159], v[70:71] op_sel_hi:[0,1]
	v_lshl_add_u64 v[176:177], s[48:49], 0, v[164:165]
	v_pk_mul_f32 v[76:77], v[46:47], v[174:175]
	v_pk_mul_f32 v[164:165], v[158:159], v[78:79] op_sel_hi:[0,1]
	v_pk_mul_f32 v[78:79], v[42:43], v[166:167]
	v_pk_mul_f32 v[80:81], v[48:49], v[172:173]
	v_pk_mul_f32 v[70:71], v[44:45], v[164:165]
	v_cvt_pk_bf16_f32 v76, v76, v77
	v_cvt_pk_bf16_f32 v77, v80, v81
	v_cvt_pk_bf16_f32 v78, v78, v79
	v_lshl_add_u64 v[176:177], v[176:177], 0, v[152:153]
	v_cvt_pk_bf16_f32 v79, v70, v71
	global_store_dwordx4 v[176:177], v[76:79], off
	v_pk_mul_f32 v[80:81], v[158:159], v[120:121] op_sel_hi:[0,1]
	v_pk_mul_f32 v[70:71], v[158:159], v[122:123] op_sel_hi:[0,1]
	v_pk_mul_f32 v[78:79], v[158:159], v[126:127] op_sel_hi:[0,1]
	v_pk_mul_f32 v[120:121], v[8:9], v[78:79]
	v_pk_mul_f32 v[76:77], v[158:159], v[118:119] op_sel_hi:[0,1]
	v_pk_mul_f32 v[126:127], v[6:7], v[80:81]
	v_pk_mul_f32 v[122:123], v[70:71], v[4:5]
	v_pk_mul_f32 v[178:179], v[76:77], v[2:3]
	v_cvt_pk_bf16_f32 v118, v126, v127
	v_cvt_pk_bf16_f32 v119, v120, v121
	v_pk_mul_f32 v[58:59], v[114:115], v[58:59] op_sel_hi:[0,1]
	v_cvt_pk_bf16_f32 v120, v178, v179
	v_cvt_pk_bf16_f32 v121, v122, v123
	global_store_dwordx4 v[176:177], v[118:121], off offset:256
	v_pk_mul_f32 v[122:123], v[46:47], v[58:59]
	v_pk_mul_f32 v[46:47], v[114:115], v[92:93] op_sel_hi:[0,1]
	v_lshlrev_b64 v[118:119], 11, v[124:125]
	v_pk_mul_f32 v[120:121], v[48:49], v[96:97]
	v_pk_mul_f32 v[48:49], v[114:115], v[90:91] op_sel_hi:[0,1]
	v_lshl_add_u64 v[118:119], s[48:49], 0, v[118:119]
	v_pk_mul_f32 v[90:91], v[44:45], v[46:47]
	v_pk_mul_f32 v[44:45], v[42:43], v[48:49]
	v_cvt_pk_bf16_f32 v42, v122, v123
	v_cvt_pk_bf16_f32 v43, v120, v121
	s_cmp_lg_u32 s46, 1
	v_cvt_pk_bf16_f32 v44, v44, v45
	v_cvt_pk_bf16_f32 v45, v90, v91
	v_lshl_add_u64 v[90:91], v[118:119], 0, v[152:153]
	global_store_dwordx4 v[90:91], v[42:45], off
	s_nop 1
	v_pk_mul_f32 v[42:43], v[114:115], v[102:103] op_sel_hi:[0,1]
	v_pk_mul_f32 v[44:45], v[114:115], v[98:99] op_sel_hi:[0,1]
	v_pk_mul_f32 v[92:93], v[8:9], v[42:43]
	v_pk_mul_f32 v[98:99], v[6:7], v[44:45]
	v_pk_mul_f32 v[6:7], v[114:115], v[100:101] op_sel_hi:[0,1]
	v_pk_mul_f32 v[8:9], v[114:115], v[94:95] op_sel_hi:[0,1]
	v_pk_mul_f32 v[94:95], v[4:5], v[6:7]
	v_pk_mul_f32 v[4:5], v[2:3], v[8:9]
	v_cvt_pk_bf16_f32 v2, v98, v99
	v_cvt_pk_bf16_f32 v3, v92, v93
	s_nop 0
	v_cvt_pk_bf16_f32 v4, v4, v5
	v_cvt_pk_bf16_f32 v5, v94, v95
	global_store_dwordx4 v[90:91], v[2:5], off offset:256
	s_cbranch_scc1 .LBB0_135
	s_ashr_i32 s35, s44, 2
	s_and_b32 s35, s35, -8
	s_lshl_b32 s31, s31, 1
	s_or_b32 s46, s35, s31
	s_lshl_b32 s31, s44, 7
	s_ashr_i32 s47, s46, 31
	s_and_b32 s31, s31, 0xf80
	s_lshl_b64 s[44:45], s[46:47], 14
	s_lshl_b64 s[48:49], s[10:11], 2
	s_add_u32 s48, s64, s48
	v_ashrrev_i32_e32 v51, 31, v50
	s_addc_u32 s49, s65, s49
	v_lshl_add_u64 v[2:3], v[50:51], 2, s[48:49]
	v_mov_b64_e32 v[90:91], v[236:237]
	v_mov_b64_e32 v[92:93], v[238:239]
	v_pk_add_f32 v[4:5], v[72:73], 0 op_sel_hi:[1,0]
	v_pk_add_f32 v[72:73], v[74:75], 0 op_sel_hi:[1,0]
	v_pk_add_f32 v[4:5], v[4:5], v[112:113]
	v_pk_add_f32 v[72:73], v[72:73], v[116:117]
	v_pk_add_f32 v[4:5], v[4:5], v[154:155]
	v_pk_add_f32 v[72:73], v[72:73], v[156:157]
	v_pk_add_f32 v[4:5], v[4:5], v[170:171]
	v_pk_add_f32 v[72:73], v[72:73], v[182:183]
	v_pk_add_f32 v[4:5], v[4:5], v[168:169]
	v_pk_add_f32 v[72:73], v[72:73], v[184:185]
	v_pk_add_f32 v[4:5], v[4:5], v[186:187]
	v_pk_add_f32 v[72:73], v[72:73], v[188:189]
	v_pk_add_f32 v[4:5], v[4:5], v[172:173]
	v_pk_add_f32 v[72:73], v[72:73], v[174:175]
	v_pk_add_f32 v[4:5], v[4:5], v[96:97]
	v_pk_add_f32 v[58:59], v[72:73], v[58:59]
	s_nop 0
	v_pk_mul_f32 v[4:5], v[4:5], v[92:93]
	v_pk_mul_f32 v[58:59], v[58:59], v[90:91]
	ds_bpermute_b32 v72, v215, v58
	ds_bpermute_b32 v73, v215, v59
	ds_bpermute_b32 v74, v215, v4
	ds_bpermute_b32 v75, v215, v5
	s_waitcnt lgkmcnt(3)
	v_add_f32_e32 v58, v58, v72
	s_waitcnt lgkmcnt(2)
	v_add_f32_e32 v59, v59, v73
	s_waitcnt lgkmcnt(1)
	v_add_f32_e32 v4, v4, v74
	s_waitcnt lgkmcnt(0)
	v_add_f32_e32 v5, v5, v75
	ds_bpermute_b32 v72, v229, v58
	ds_bpermute_b32 v73, v229, v59
	ds_bpermute_b32 v74, v229, v4
	ds_bpermute_b32 v75, v229, v5
	s_waitcnt lgkmcnt(3)
	v_add_f32_e32 v58, v58, v72
	s_waitcnt lgkmcnt(2)
	v_add_f32_e32 v59, v59, v73
	s_waitcnt lgkmcnt(1)
	v_add_f32_e32 v72, v4, v74
	s_waitcnt lgkmcnt(0)
	v_add_f32_e32 v73, v5, v75
	ds_bpermute_b32 v4, v230, v58
	ds_bpermute_b32 v5, v230, v59
	ds_bpermute_b32 v74, v230, v72
	ds_bpermute_b32 v75, v230, v73
	s_waitcnt lgkmcnt(3)
	v_add_f32_e32 v4, v58, v4
	s_waitcnt lgkmcnt(2)
	v_add_f32_e32 v5, v59, v5
	s_waitcnt lgkmcnt(1)
	v_add_f32_e32 v58, v72, v74
	s_waitcnt lgkmcnt(0)
	v_add_f32_e32 v74, v73, v75
	ds_bpermute_b32 v59, v231, v4
	ds_bpermute_b32 v72, v231, v5
	ds_bpermute_b32 v73, v231, v58
	ds_bpermute_b32 v75, v231, v74
	s_and_saveexec_b64 s[48:49], s[6:7]
	s_cbranch_execz .LBB0_128
	s_add_u32 s10, s0, s44
	s_addc_u32 s35, s1, s45
	s_lshl_b32 s47, s31, 2
	s_add_u32 s10, s10, s47
	s_addc_u32 s35, s35, 0
	s_lshl_b32 s47, s60, 2
	s_add_u32 s50, s10, s47
	s_waitcnt lgkmcnt(3)
	v_add_f32_e32 v59, v4, v59
	s_addc_u32 s51, s35, 0
	s_waitcnt lgkmcnt(2)
	v_add_f32_e32 v72, v5, v72
	v_lshl_add_u64 v[4:5], v[50:51], 2, s[50:51]
	v_mul_f32_e32 v59, 0x3b800000, v59
	s_waitcnt lgkmcnt(1)
	v_add_f32_e32 v58, v58, v73
	global_atomic_add_f32 v[4:5], v59, off
	v_mul_f32_e32 v59, 0x3b800000, v72
	s_waitcnt lgkmcnt(0)
	v_add_f32_e32 v74, v74, v75
	global_atomic_add_f32 v[4:5], v59, off offset:4
	v_mul_f32_e32 v58, 0x3b800000, v58
	global_atomic_add_f32 v[4:5], v58, off offset:8
	v_mul_f32_e32 v58, 0x3b800000, v74
	global_atomic_add_f32 v[4:5], v58, off offset:12
.LBB0_128:
	s_or_b64 exec, exec, s[48:49]
	s_waitcnt lgkmcnt(0)
	v_mov_b64_e32 v[72:73], v[240:241]
	v_mov_b64_e32 v[74:75], v[242:243]
	v_pk_add_f32 v[4:5], v[34:35], 0 op_sel_hi:[1,0]
	v_pk_add_f32 v[34:35], v[36:37], 0 op_sel_hi:[1,0]
	v_pk_add_f32 v[4:5], v[4:5], v[56:57]
	v_pk_add_f32 v[34:35], v[34:35], v[60:61]
	v_pk_add_f32 v[4:5], v[4:5], v[82:83]
	v_pk_add_f32 v[34:35], v[34:35], v[84:85]
	v_pk_add_f32 v[4:5], v[4:5], v[108:109]
	v_pk_add_f32 v[34:35], v[34:35], v[110:111]
	v_pk_add_f32 v[4:5], v[4:5], v[128:129]
	v_pk_add_f32 v[34:35], v[34:35], v[150:151]
	v_pk_add_f32 v[4:5], v[4:5], v[160:161]
	v_pk_add_f32 v[34:35], v[34:35], v[162:163]
	v_pk_add_f32 v[4:5], v[4:5], v[164:165]
	v_pk_add_f32 v[34:35], v[34:35], v[166:167]
	v_pk_add_f32 v[4:5], v[4:5], v[46:47]
	v_pk_add_f32 v[34:35], v[34:35], v[48:49]
	s_nop 0
	v_pk_mul_f32 v[4:5], v[4:5], v[74:75]
	v_pk_mul_f32 v[34:35], v[34:35], v[72:73]
	ds_bpermute_b32 v36, v215, v34
	ds_bpermute_b32 v37, v215, v35
	ds_bpermute_b32 v46, v215, v4
	ds_bpermute_b32 v47, v215, v5
	s_waitcnt lgkmcnt(3)
	v_add_f32_e32 v34, v34, v36
	s_waitcnt lgkmcnt(2)
	v_add_f32_e32 v35, v35, v37
	s_waitcnt lgkmcnt(1)
	v_add_f32_e32 v4, v4, v46
	s_waitcnt lgkmcnt(0)
	v_add_f32_e32 v5, v5, v47
	ds_bpermute_b32 v36, v229, v34
	ds_bpermute_b32 v37, v229, v35
	ds_bpermute_b32 v46, v229, v4
	ds_bpermute_b32 v47, v229, v5
	s_waitcnt lgkmcnt(3)
	v_add_f32_e32 v34, v34, v36
	s_waitcnt lgkmcnt(2)
	v_add_f32_e32 v35, v35, v37
	s_waitcnt lgkmcnt(1)
	v_add_f32_e32 v36, v4, v46
	s_waitcnt lgkmcnt(0)
	v_add_f32_e32 v37, v5, v47
	ds_bpermute_b32 v4, v230, v34
	ds_bpermute_b32 v5, v230, v35
	ds_bpermute_b32 v46, v230, v36
	ds_bpermute_b32 v47, v230, v37
	s_waitcnt lgkmcnt(3)
	v_add_f32_e32 v4, v34, v4
	s_waitcnt lgkmcnt(2)
	v_add_f32_e32 v5, v35, v5
	s_waitcnt lgkmcnt(1)
	v_add_f32_e32 v34, v36, v46
	s_waitcnt lgkmcnt(0)
	v_add_f32_e32 v46, v37, v47
	ds_bpermute_b32 v35, v231, v4
	ds_bpermute_b32 v36, v231, v5
	ds_bpermute_b32 v37, v231, v34
	ds_bpermute_b32 v47, v231, v46
	s_and_saveexec_b64 s[48:49], s[6:7]
	s_cbranch_execz .LBB0_130
	s_add_u32 s10, s0, s44
	s_addc_u32 s35, s1, s45
	s_lshl_b32 s44, s31, 2
	s_add_u32 s10, s10, s44
	s_addc_u32 s35, s35, 0
	s_lshl_b32 s44, s60, 2
	s_add_u32 s44, s10, s44
	s_waitcnt lgkmcnt(3)
	v_add_f32_e32 v35, v4, v35
	s_addc_u32 s45, s35, 0
	s_waitcnt lgkmcnt(2)
	v_add_f32_e32 v36, v5, v36
	v_lshl_add_u64 v[4:5], v[50:51], 2, s[44:45]
	v_mul_f32_e32 v35, 0x3b800000, v35
	s_waitcnt lgkmcnt(1)
	v_add_f32_e32 v34, v34, v37
	global_atomic_add_f32 v[4:5], v35, off offset:16
	v_mul_f32_e32 v35, 0x3b800000, v36
	s_waitcnt lgkmcnt(0)
	v_add_f32_e32 v46, v46, v47
	global_atomic_add_f32 v[4:5], v35, off offset:20
	v_mul_f32_e32 v34, 0x3b800000, v34
	global_atomic_add_f32 v[4:5], v34, off offset:24
	v_mul_f32_e32 v34, 0x3b800000, v46
	global_atomic_add_f32 v[4:5], v34, off offset:28
.LBB0_130:
	s_or_b64 exec, exec, s[48:49]
	s_waitcnt lgkmcnt(1)
	v_mov_b64_e32 v[34:35], v[244:245]
	v_mov_b64_e32 v[36:37], v[246:247]
	v_pk_add_f32 v[4:5], v[20:21], 0 op_sel_hi:[1,0]
	v_pk_add_f32 v[20:21], v[24:25], 0 op_sel_hi:[1,0]
	v_pk_add_f32 v[4:5], v[4:5], v[30:31]
	v_pk_add_f32 v[20:21], v[20:21], v[32:33]
	v_pk_add_f32 v[4:5], v[4:5], v[52:53]
	v_pk_add_f32 v[20:21], v[20:21], v[54:55]
	v_pk_add_f32 v[4:5], v[4:5], v[66:67]
	v_pk_add_f32 v[20:21], v[20:21], v[68:69]
	v_pk_add_f32 v[4:5], v[4:5], v[86:87]
	v_pk_add_f32 v[20:21], v[20:21], v[88:89]
	v_pk_add_f32 v[4:5], v[4:5], v[104:105]
	v_pk_add_f32 v[20:21], v[20:21], v[106:107]
	v_pk_add_f32 v[4:5], v[4:5], v[78:79]
	v_pk_add_f32 v[20:21], v[20:21], v[80:81]
	v_pk_add_f32 v[4:5], v[4:5], v[42:43]
	v_pk_add_f32 v[20:21], v[20:21], v[44:45]
	s_or_b32 s44, s46, 1
	s_ashr_i32 s45, s44, 31
	s_lshl_b64 s[44:45], s[44:45], 14
	s_nop 0
	v_pk_mul_f32 v[4:5], v[4:5], v[36:37]
	v_pk_mul_f32 v[20:21], v[20:21], v[34:35]
	ds_bpermute_b32 v24, v215, v20
	ds_bpermute_b32 v25, v215, v21
	ds_bpermute_b32 v30, v215, v4
	ds_bpermute_b32 v31, v215, v5
	s_waitcnt lgkmcnt(3)
	v_add_f32_e32 v20, v20, v24
	s_waitcnt lgkmcnt(2)
	v_add_f32_e32 v21, v21, v25
	s_waitcnt lgkmcnt(1)
	v_add_f32_e32 v4, v4, v30
	s_waitcnt lgkmcnt(0)
	v_add_f32_e32 v5, v5, v31
	ds_bpermute_b32 v24, v229, v20
	ds_bpermute_b32 v25, v229, v21
	ds_bpermute_b32 v30, v229, v4
	ds_bpermute_b32 v31, v229, v5
	s_waitcnt lgkmcnt(3)
	v_add_f32_e32 v20, v20, v24
	s_waitcnt lgkmcnt(2)
	v_add_f32_e32 v21, v21, v25
	s_waitcnt lgkmcnt(1)
	v_add_f32_e32 v24, v4, v30
	s_waitcnt lgkmcnt(0)
	v_add_f32_e32 v25, v5, v31
	ds_bpermute_b32 v4, v230, v20
	ds_bpermute_b32 v5, v230, v21
	ds_bpermute_b32 v30, v230, v24
	ds_bpermute_b32 v31, v230, v25
	s_waitcnt lgkmcnt(3)
	v_add_f32_e32 v4, v20, v4
	s_waitcnt lgkmcnt(2)
	v_add_f32_e32 v5, v21, v5
	s_waitcnt lgkmcnt(1)
	v_add_f32_e32 v20, v24, v30
	s_waitcnt lgkmcnt(0)
	v_add_f32_e32 v30, v25, v31
	ds_bpermute_b32 v21, v231, v4
	ds_bpermute_b32 v24, v231, v5
	ds_bpermute_b32 v25, v231, v20
	ds_bpermute_b32 v31, v231, v30
	s_and_saveexec_b64 s[46:47], s[6:7]
	s_cbranch_execz .LBB0_132
	s_add_u32 s10, s0, s44
	s_addc_u32 s35, s1, s45
	s_lshl_b32 s48, s31, 2
	s_add_u32 s10, s10, s48
	s_addc_u32 s35, s35, 0
	s_lshl_b32 s48, s60, 2
	s_add_u32 s48, s10, s48
	s_waitcnt lgkmcnt(3)
	v_add_f32_e32 v21, v4, v21
	s_addc_u32 s49, s35, 0
	s_waitcnt lgkmcnt(2)
	v_add_f32_e32 v24, v5, v24
	v_lshl_add_u64 v[4:5], v[50:51], 2, s[48:49]
	v_mul_f32_e32 v21, 0x3b800000, v21
	s_waitcnt lgkmcnt(1)
	v_add_f32_e32 v20, v20, v25
	global_atomic_add_f32 v[4:5], v21, off
	v_mul_f32_e32 v21, 0x3b800000, v24
	s_waitcnt lgkmcnt(0)
	v_add_f32_e32 v30, v30, v31
	global_atomic_add_f32 v[4:5], v21, off offset:4
	v_mul_f32_e32 v20, 0x3b800000, v20
	global_atomic_add_f32 v[4:5], v20, off offset:8
	v_mul_f32_e32 v20, 0x3b800000, v30
	global_atomic_add_f32 v[4:5], v20, off offset:12
.LBB0_132:
	s_or_b64 exec, exec, s[46:47]
	v_mov_b64_e32 v[2:3], v[248:249]
	v_mov_b64_e32 v[4:5], v[250:251]
	v_pk_add_f32 v[10:11], v[10:11], 0 op_sel_hi:[1,0]
	v_pk_add_f32 v[12:13], v[12:13], 0 op_sel_hi:[1,0]
	v_pk_add_f32 v[10:11], v[10:11], v[14:15]
	v_pk_add_f32 v[12:13], v[12:13], v[16:17]
	v_pk_add_f32 v[10:11], v[10:11], v[18:19]
	v_pk_add_f32 v[12:13], v[12:13], v[22:23]
	v_pk_add_f32 v[10:11], v[10:11], v[26:27]
	v_pk_add_f32 v[12:13], v[12:13], v[28:29]
	v_pk_add_f32 v[10:11], v[10:11], v[38:39]
	v_pk_add_f32 v[12:13], v[12:13], v[40:41]
	v_pk_add_f32 v[10:11], v[10:11], v[62:63]
	v_pk_add_f32 v[12:13], v[12:13], v[64:65]
	v_pk_add_f32 v[10:11], v[10:11], v[70:71]
	v_pk_add_f32 v[12:13], v[12:13], v[76:77]
	v_pk_add_f32 v[6:7], v[10:11], v[6:7]
	v_pk_add_f32 v[8:9], v[12:13], v[8:9]
	s_nop 0
	v_pk_mul_f32 v[4:5], v[6:7], v[4:5]
	v_pk_mul_f32 v[2:3], v[8:9], v[2:3]
	ds_bpermute_b32 v6, v215, v2
	ds_bpermute_b32 v7, v215, v3
	ds_bpermute_b32 v8, v215, v4
	ds_bpermute_b32 v9, v215, v5
	s_waitcnt lgkmcnt(3)
	v_add_f32_e32 v2, v2, v6
	s_waitcnt lgkmcnt(2)
	v_add_f32_e32 v3, v3, v7
	s_waitcnt lgkmcnt(1)
	v_add_f32_e32 v4, v4, v8
	s_waitcnt lgkmcnt(0)
	v_add_f32_e32 v5, v5, v9
	ds_bpermute_b32 v6, v229, v2
	ds_bpermute_b32 v7, v229, v3
	ds_bpermute_b32 v8, v229, v4
	ds_bpermute_b32 v9, v229, v5
	s_waitcnt lgkmcnt(3)
	v_add_f32_e32 v2, v2, v6
	s_waitcnt lgkmcnt(2)
	v_add_f32_e32 v3, v3, v7
	s_waitcnt lgkmcnt(1)
	v_add_f32_e32 v4, v4, v8
	s_waitcnt lgkmcnt(0)
	v_add_f32_e32 v5, v5, v9
	ds_bpermute_b32 v6, v230, v2
	ds_bpermute_b32 v7, v230, v3
	ds_bpermute_b32 v8, v230, v4
	ds_bpermute_b32 v9, v230, v5
	s_waitcnt lgkmcnt(3)
	v_add_f32_e32 v2, v2, v6
	s_waitcnt lgkmcnt(2)
	v_add_f32_e32 v3, v3, v7
	s_waitcnt lgkmcnt(1)
	v_add_f32_e32 v4, v4, v8
	s_waitcnt lgkmcnt(0)
	v_add_f32_e32 v8, v5, v9
	ds_bpermute_b32 v5, v231, v2
	ds_bpermute_b32 v6, v231, v3
	ds_bpermute_b32 v7, v231, v4
	ds_bpermute_b32 v9, v231, v8
	s_and_saveexec_b64 s[46:47], s[6:7]
	s_cbranch_execz .LBB0_134
	s_add_u32 s10, s0, s44
	s_addc_u32 s35, s1, s45
	s_lshl_b32 s31, s31, 2
	s_add_u32 s10, s10, s31
	s_addc_u32 s31, s35, 0
	s_lshl_b32 s35, s60, 2
	s_add_u32 s44, s10, s35
	s_waitcnt lgkmcnt(3)
	v_add_f32_e32 v5, v2, v5
	s_addc_u32 s45, s31, 0
	s_waitcnt lgkmcnt(2)
	v_add_f32_e32 v6, v3, v6
	v_lshl_add_u64 v[2:3], v[50:51], 2, s[44:45]
	v_mul_f32_e32 v5, 0x3b800000, v5
	s_waitcnt lgkmcnt(1)
	v_add_f32_e32 v4, v4, v7
	global_atomic_add_f32 v[2:3], v5, off offset:16
	v_mul_f32_e32 v5, 0x3b800000, v6
	s_waitcnt lgkmcnt(0)
	v_add_f32_e32 v8, v8, v9
	global_atomic_add_f32 v[2:3], v5, off offset:20
	v_mul_f32_e32 v4, 0x3b800000, v4
	global_atomic_add_f32 v[2:3], v4, off offset:24
	v_mul_f32_e32 v4, 0x3b800000, v8
	global_atomic_add_f32 v[2:3], v4, off offset:28

.LBB0_514:
	s_ashr_i32 s0, s55, 10
	s_lshl_b32 s1, s0, 25
	s_lshl_b32 s0, s0, 18
	v_add_u32_e32 v4, s78, v206
	v_lshl_add_u32 v5, v4, 3, s0
	s_lshl_b32 s0, s78, 10
	s_or_b32 s0, s0, s1
	s_lshl_b32 s1, s59, 20
	s_or_b32 s0, s0, s1
	v_lshl_add_u32 v4, v206, 7, s0
	s_nop 0
	v_or_b32_e32 v6, s59, v5
	v_cmp_lt_i32_e64 s[6:7], -1, v4
	v_cmp_gt_u32_e64 s[8:9], 32, v205
	v_cmp_lt_f32_e32 vcc, 0, v3
	s_and_b64 s[76:77], s[6:7], s[8:9]
	v_ashrrev_i32_e32 v7, 31, v6
	s_and_saveexec_b64 s[78:79], s[76:77]
	v_readlane_b32 s92, v255, 35
	v_readlane_b32 s90, v255, 33
	v_readlane_b32 s93, v255, 36
	v_readlane_b32 s94, v255, 37
	v_readlane_b32 s91, v255, 34
	v_readlane_b32 s95, v255, 38
	s_cbranch_execz .LBB0_516
	s_mov_b32 s0, 0x800000
	v_cmp_gt_f32_e64 s[8:9], s0, v3
	v_readlane_b32 s0, v255, 27
	v_readlane_b32 s1, v255, 28
	v_cndmask_b32_e64 v8, 0, 32, s[8:9]
	v_ldexp_f32 v8, v3, v8
	v_log_f32_e32 v10, v8
	v_cndmask_b32_e64 v5, 0, v177, s[8:9]
	v_lshl_add_u64 v[8:9], v[6:7], 2, s[0:1]
	v_sub_f32_e32 v5, v10, v5
	v_add_f32_e32 v5, v207, v5
	v_cndmask_b32_e32 v5, v175, v5, vcc
	global_store_dword v[8:9], v5, off

.LBB0_657:
	s_nop 0
	s_add_i32 s53, s10, s28
	s_cmpk_gt_i32 s53, 0x7ff
	s_cselect_b64 s[60:61], -1, 0
	s_cmpk_lt_i32 s53, 0x800
	s_cselect_b64 s[12:13], -1, 0
	s_and_b64 s[0:1], s[12:13], exec
	s_cselect_b32 s8, s53, s10
	s_cmpk_gt_i32 s8, 0x3ff
	s_cbranch_scc0 .LBB0_659
	s_lshl_b32 s0, s8, 8
	s_and_b32 s9, s0, 0x100
	s_lshl_b32 s0, s8, 15
	s_lshl_b32 s1, s8, 2
	s_and_b32 s0, s0, 0xff800000
	s_and_b32 s1, s1, 0x380
	s_or_b32 s0, s0, s1
	s_add_i32 s76, s0, 0xfe000000
	s_bfe_u32 s2, s8, 0x40001
	s_lshl_b64 s[6:7], s[76:77], 1
	v_readlane_b32 s0, v255, 20
	v_readlane_b32 s1, v255, 21
	s_add_u32 s0, s0, s6
	s_addc_u32 s1, s1, s7
	v_readlane_b32 s11, v255, 22
	s_add_u32 s62, s11, s6
	s_addc_u32 s63, s25, s7
	s_add_u32 s66, s3, s6
	s_addc_u32 s67, s33, s7
	v_add_u32_e32 v3, s9, v1
	s_lshl_b32 s6, s2, 10
	v_lshl_or_b32 v184, v3, 14, s6
	s_lshl_b32 s6, s9, 4
	s_or_b32 s2, s6, s2
	s_add_i32 s46, s2, 0xfffff800
	s_lshr_b32 s2, s9, 7
	s_xor_b32 s64, s2, 2
	s_mov_b32 s47, 16
	s_cbranch_execz .LBB0_660
	s_branch .LBB0_661

.LBB0_699:
	v_ashrrev_i32_e32 v183, 31, v182
	v_readlane_b32 s10, v255, 23
	s_waitcnt vmcnt(0)
	v_and_b32_e32 v178, 0xff800000, v182
	v_bfe_u32 v179, v182, 7, 3
	v_lshl_or_b32 v178, v179, 20, v178
	v_bfe_u32 v179, v182, 10, 13
	v_lshl_or_b32 v178, v179, 7, v178
	v_cndmask_b32_e64 v178, 0, v178, s[74:75]
	v_mov_b32_e32 v179, 0
	s_nop 0
	v_mul_f32_e32 v104, v3, v106
	v_lshlrev_b32_e32 v108, 3, v199
	v_readlane_b32 s11, v255, 24
	v_ashrrev_i32_e32 v109, 31, v108
	v_pk_mul_f32 v[110:111], v[70:71], v[104:105] op_sel_hi:[1,0]
	v_lshl_add_u64 v[70:71], s[10:11], 0, v[178:179]
	v_pk_mul_f32 v[66:67], v[66:67], v[104:105] op_sel_hi:[1,0]
	v_pk_mul_f32 v[68:69], v[68:69], v[104:105] op_sel_hi:[1,0]
	v_pk_mul_f32 v[112:113], v[72:73], v[104:105] op_sel_hi:[1,0]
	v_pk_mul_f32 v[106:107], v[74:75], v[104:105] op_sel_hi:[1,0]
	v_pk_mul_f32 v[76:77], v[76:77], v[104:105] op_sel_hi:[1,0]
	v_pk_mul_f32 v[78:79], v[78:79], v[104:105] op_sel_hi:[1,0]
	v_pk_mul_f32 v[80:81], v[80:81], v[104:105] op_sel_hi:[1,0]
	s_and_b64 vcc, exec, s[8:9]
	v_lshl_add_u64 v[72:73], v[70:71], 0, v[108:109]
	s_cbranch_vccnz .LBB0_701
	global_load_dwordx2 v[70:71], v[72:73], off
	global_load_dwordx2 v[74:75], v[72:73], off offset:16
	s_waitcnt vmcnt(1)
	v_mov_b32_e32 v3, v71
	s_waitcnt vmcnt(0)
	v_mov_b32_e32 v17, v75
	v_permlane32_swap_b32_e32 v70, v3
	s_nop 0
	v_permlane32_swap_b32_e32 v74, v17
	v_cvt_f32_i32_sdwa v181, sext(v70) dst_sel:DWORD dst_unused:UNUSED_PAD src0_sel:BYTE_1
	v_cvt_f32_i32_sdwa v180, sext(v70) dst_sel:DWORD dst_unused:UNUSED_PAD src0_sel:BYTE_0
	v_cvt_f32_i32_sdwa v71, sext(v70) dst_sel:DWORD dst_unused:UNUSED_PAD src0_sel:BYTE_3
	v_cvt_f32_i32_sdwa v70, sext(v70) dst_sel:DWORD dst_unused:UNUSED_PAD src0_sel:BYTE_2
	v_cvt_f32_i32_sdwa v187, sext(v3) dst_sel:DWORD dst_unused:UNUSED_PAD src0_sel:BYTE_1
	v_cvt_f32_i32_sdwa v186, sext(v3) dst_sel:DWORD dst_unused:UNUSED_PAD src0_sel:BYTE_0
	v_cvt_f32_i32_sdwa v189, sext(v3) dst_sel:DWORD dst_unused:UNUSED_PAD src0_sel:BYTE_3
	v_cvt_f32_i32_sdwa v188, sext(v3) dst_sel:DWORD dst_unused:UNUSED_PAD src0_sel:BYTE_2
	v_cvt_f32_i32_sdwa v191, sext(v74) dst_sel:DWORD dst_unused:UNUSED_PAD src0_sel:BYTE_1
	v_cvt_f32_i32_sdwa v190, sext(v74) dst_sel:DWORD dst_unused:UNUSED_PAD src0_sel:BYTE_0
	v_cvt_f32_i32_sdwa v75, sext(v74) dst_sel:DWORD dst_unused:UNUSED_PAD src0_sel:BYTE_3
	v_cvt_f32_i32_sdwa v74, sext(v74) dst_sel:DWORD dst_unused:UNUSED_PAD src0_sel:BYTE_2
	v_cvt_f32_i32_sdwa v193, sext(v17) dst_sel:DWORD dst_unused:UNUSED_PAD src0_sel:BYTE_1
	v_cvt_f32_i32_sdwa v192, sext(v17) dst_sel:DWORD dst_unused:UNUSED_PAD src0_sel:BYTE_0
	v_cvt_f32_i32_sdwa v197, sext(v17) dst_sel:DWORD dst_unused:UNUSED_PAD src0_sel:BYTE_3
	v_cvt_f32_i32_sdwa v196, sext(v17) dst_sel:DWORD dst_unused:UNUSED_PAD src0_sel:BYTE_2
	v_pk_fma_f32 v[76:77], v[102:103], v[74:75], v[76:77] op_sel_hi:[0,1,1]
	v_pk_fma_f32 v[78:79], v[102:103], v[192:193], v[78:79] op_sel_hi:[0,1,1]
	v_pk_fma_f32 v[106:107], v[102:103], v[190:191], v[106:107] op_sel_hi:[0,1,1]
	v_pk_fma_f32 v[80:81], v[102:103], v[196:197], v[80:81] op_sel_hi:[0,1,1]
	v_pk_fma_f32 v[112:113], v[102:103], v[188:189], v[112:113] op_sel_hi:[0,1,1]
	v_pk_fma_f32 v[110:111], v[102:103], v[186:187], v[110:111] op_sel_hi:[0,1,1]
	v_pk_fma_f32 v[68:69], v[102:103], v[70:71], v[68:69] op_sel_hi:[0,1,1]
	v_pk_fma_f32 v[66:67], v[102:103], v[180:181], v[66:67] op_sel_hi:[0,1,1]

.LBB0_765:
	v_ashrrev_i32_e32 v183, 31, v182
	v_and_b32_e32 v88, 0xff800000, v182
	v_bfe_u32 v89, v182, 7, 3
	v_lshl_or_b32 v88, v89, 20, v88
	v_bfe_u32 v89, v182, 10, 13
	v_lshl_or_b32 v88, v89, 7, v88
	v_cndmask_b32_e64 v88, 0, v88, s[74:75]
	v_mov_b32_e32 v89, 0
	s_nop 0
	v_lshlrev_b32_e32 v4, 3, v179
	v_mul_f32_e32 v14, v3, v7
	v_ashrrev_i32_e32 v5, 31, v4
	v_lshl_add_u64 v[16:17], s[16:17], 0, v[88:89]
	v_pk_mul_f32 v[6:7], v[66:67], v[14:15] op_sel_hi:[1,0]
	v_pk_mul_f32 v[82:83], v[68:69], v[14:15] op_sel_hi:[1,0]
	v_pk_mul_f32 v[84:85], v[70:71], v[14:15] op_sel_hi:[1,0]
	v_pk_mul_f32 v[86:87], v[72:73], v[14:15] op_sel_hi:[1,0]
	v_pk_mul_f32 v[72:73], v[74:75], v[14:15] op_sel_hi:[1,0]
	v_pk_mul_f32 v[74:75], v[76:77], v[14:15] op_sel_hi:[1,0]
	v_pk_mul_f32 v[76:77], v[78:79], v[14:15] op_sel_hi:[1,0]
	v_pk_mul_f32 v[78:79], v[80:81], v[14:15] op_sel_hi:[1,0]
	s_and_b64 vcc, exec, s[10:11]
	v_lshl_add_u64 v[16:17], v[16:17], 0, v[4:5]
	s_cbranch_vccnz .LBB0_767
	global_load_dwordx2 v[66:67], v[16:17], off
	global_load_dwordx2 v[68:69], v[16:17], off offset:16
	s_waitcnt vmcnt(1)
	v_mov_b32_e32 v3, v67
	s_waitcnt vmcnt(0)
	v_mov_b32_e32 v9, v69
	v_permlane32_swap_b32_e32 v66, v3
	s_nop 0
	v_permlane32_swap_b32_e32 v68, v9
	v_cvt_f32_i32_sdwa v71, sext(v66) dst_sel:DWORD dst_unused:UNUSED_PAD src0_sel:BYTE_1
	v_cvt_f32_i32_sdwa v70, sext(v66) dst_sel:DWORD dst_unused:UNUSED_PAD src0_sel:BYTE_0
	v_cvt_f32_i32_sdwa v67, sext(v66) dst_sel:DWORD dst_unused:UNUSED_PAD src0_sel:BYTE_3
	v_cvt_f32_i32_sdwa v66, sext(v66) dst_sel:DWORD dst_unused:UNUSED_PAD src0_sel:BYTE_2
	v_cvt_f32_i32_sdwa v81, sext(v3) dst_sel:DWORD dst_unused:UNUSED_PAD src0_sel:BYTE_1
	v_cvt_f32_i32_sdwa v80, sext(v3) dst_sel:DWORD dst_unused:UNUSED_PAD src0_sel:BYTE_0
	v_cvt_f32_i32_sdwa v91, sext(v3) dst_sel:DWORD dst_unused:UNUSED_PAD src0_sel:BYTE_3
	v_cvt_f32_i32_sdwa v90, sext(v3) dst_sel:DWORD dst_unused:UNUSED_PAD src0_sel:BYTE_2
	v_cvt_f32_i32_sdwa v93, sext(v68) dst_sel:DWORD dst_unused:UNUSED_PAD src0_sel:BYTE_1
	v_cvt_f32_i32_sdwa v92, sext(v68) dst_sel:DWORD dst_unused:UNUSED_PAD src0_sel:BYTE_0
	v_cvt_f32_i32_sdwa v69, sext(v68) dst_sel:DWORD dst_unused:UNUSED_PAD src0_sel:BYTE_3
	v_cvt_f32_i32_sdwa v68, sext(v68) dst_sel:DWORD dst_unused:UNUSED_PAD src0_sel:BYTE_2
	v_cvt_f32_i32_sdwa v95, sext(v9) dst_sel:DWORD dst_unused:UNUSED_PAD src0_sel:BYTE_1
	v_cvt_f32_i32_sdwa v94, sext(v9) dst_sel:DWORD dst_unused:UNUSED_PAD src0_sel:BYTE_0
	v_cvt_f32_i32_sdwa v97, sext(v9) dst_sel:DWORD dst_unused:UNUSED_PAD src0_sel:BYTE_3
	v_cvt_f32_i32_sdwa v96, sext(v9) dst_sel:DWORD dst_unused:UNUSED_PAD src0_sel:BYTE_2
	v_pk_fma_f32 v[74:75], v[12:13], v[68:69], v[74:75] op_sel_hi:[0,1,1]
	v_pk_fma_f32 v[76:77], v[12:13], v[94:95], v[76:77] op_sel_hi:[0,1,1]
	v_pk_fma_f32 v[72:73], v[12:13], v[92:93], v[72:73] op_sel_hi:[0,1,1]
	v_pk_fma_f32 v[78:79], v[12:13], v[96:97], v[78:79] op_sel_hi:[0,1,1]
	v_pk_fma_f32 v[86:87], v[12:13], v[90:91], v[86:87] op_sel_hi:[0,1,1]
	v_pk_fma_f32 v[84:85], v[12:13], v[80:81], v[84:85] op_sel_hi:[0,1,1]
	v_pk_fma_f32 v[82:83], v[12:13], v[66:67], v[82:83] op_sel_hi:[0,1,1]
	v_pk_fma_f32 v[6:7], v[12:13], v[70:71], v[6:7] op_sel_hi:[0,1,1]

.LBB0_883:
	v_mov_b32_e32 v84, 0
	v_mov_b32_e32 v82, 0
	v_cvt_f32_i32_e32 v155, v155
	v_add_u32_e32 v82, v82, v1
	v_lshl_add_u32 v82, v82, 3, s67
	v_lshl_add_u32 v190, s42, 7, v82
	s_lshl_b32 s42, s42, 8
	s_ashr_i32 s43, s42, 31
	s_lshl_b64 s[42:43], s[42:43], 2
	s_add_u32 s42, s65, s42
	s_addc_u32 s43, s66, s43
	s_lshl_b32 s2, s52, 8
	v_add3_u32 v182, s2, v184, v84
	v_ashrrev_i32_e32 v191, 31, v190
	v_ashrrev_i32_e32 v83, 31, v82
	v_ashrrev_i32_e32 v183, 31, v182
	v_lshlrev_b64 v[90:91], 2, v[190:191]
	v_lshl_add_u64 v[86:87], v[82:83], 2, s[42:43]
	v_lshl_add_u64 v[82:83], v[182:183], 2, s[12:13]
	v_lshl_add_u64 v[92:93], s[4:5], 0, v[90:91]
	global_load_dword v189, v[82:83], off
	global_load_dword v198, v[82:83], off offset:64
	global_load_dword v199, v[82:83], off offset:128
	global_load_dword v200, v[82:83], off offset:192
	global_load_dword v201, v[82:83], off offset:512
	global_load_dword v202, v[82:83], off offset:576
	global_load_dword v203, v[82:83], off offset:640
	global_load_dword v204, v[82:83], off offset:704
	global_load_dwordx4 v[94:97], v[86:87], off offset:16
	global_load_dwordx4 v[106:109], v[86:87], off
	s_nop 0
	global_load_dwordx4 v[82:85], v[86:87], off offset:528
	s_nop 0
	global_load_dwordx4 v[86:89], v[86:87], off offset:512
	s_nop 0
	global_load_dwordx4 v[102:105], v[92:93], off offset:16
	global_load_dwordx4 v[110:113], v[92:93], off
	v_lshl_add_u64 v[90:91], s[30:31], 0, v[90:91]
	global_load_dwordx4 v[98:101], v[90:91], off
	s_nop 0
	global_load_dwordx4 v[90:93], v[90:91], off offset:16
	v_cvt_f32_i32_e32 v154, v154
	v_cvt_f32_i32_e32 v158, v158
	v_cvt_f32_i32_e32 v147, v147
	v_cvt_f32_i32_e32 v146, v146
	v_cvt_f32_i32_e32 v150, v150
	v_cvt_f32_i32_e32 v160, v160
	v_cvt_f32_i32_e32 v156, v156
	v_cvt_f32_i32_e32 v152, v152
	v_cvt_f32_i32_e32 v148, v148
	v_cvt_f32_i32_e32 v159, v159
	v_cvt_f32_i32_e32 v161, v161
	v_cvt_f32_i32_e32 v157, v157
	v_cvt_f32_i32_e32 v153, v153
	v_cvt_f32_i32_e32 v151, v151
	v_cvt_f32_i32_e32 v149, v149
	v_cvt_f32_i32_e32 v142, v142
	v_cvt_f32_i32_e32 v138, v138
	v_cvt_f32_i32_e32 v134, v134
	v_cvt_f32_i32_e32 v130, v130
	v_cvt_f32_i32_e32 v143, v143
	v_cvt_f32_i32_e32 v139, v139
	v_cvt_f32_i32_e32 v135, v135
	v_cvt_f32_i32_e32 v131, v131
	v_cvt_f32_i32_e32 v144, v144
	v_cvt_f32_i32_e32 v140, v140
	v_cvt_f32_i32_e32 v136, v136
	v_cvt_f32_i32_e32 v132, v132
	v_cvt_f32_i32_e32 v145, v145
	v_cvt_f32_i32_e32 v141, v141
	v_cvt_f32_i32_e32 v137, v137
	v_cvt_f32_i32_e32 v133, v133
	v_cvt_f32_i32_e32 v126, v126
	v_cvt_f32_i32_e32 v122, v122
	v_cvt_f32_i32_e32 v118, v118
	v_cvt_f32_i32_e32 v114, v114
	v_cvt_f32_i32_e32 v127, v127
	v_cvt_f32_i32_e32 v123, v123
	v_cvt_f32_i32_e32 v119, v119
	v_cvt_f32_i32_e32 v115, v115
	v_cvt_f32_i32_e32 v128, v128
	v_cvt_f32_i32_e32 v124, v124
	v_cvt_f32_i32_e32 v120, v120
	v_cvt_f32_i32_e32 v116, v116
	v_cvt_f32_i32_e32 v129, v129
	v_cvt_f32_i32_e32 v125, v125
	v_cvt_f32_i32_e32 v121, v121
	v_cvt_f32_i32_e32 v117, v117
	v_cvt_f32_i32_e32 v78, v78
	v_cvt_f32_i32_e32 v74, v74
	v_cvt_f32_i32_e32 v70, v70
	v_cvt_f32_i32_e32 v66, v66
	v_cvt_f32_i32_e32 v79, v79
	v_cvt_f32_i32_e32 v75, v75
	v_cvt_f32_i32_e32 v71, v71
	v_cvt_f32_i32_e32 v67, v67
	v_cvt_f32_i32_e32 v80, v80
	v_cvt_f32_i32_e32 v76, v76
	v_cvt_f32_i32_e32 v72, v72
	v_cvt_f32_i32_e32 v68, v68
	v_cvt_f32_i32_e32 v81, v81
	v_cvt_f32_i32_e32 v77, v77
	v_cvt_f32_i32_e32 v73, v73
	v_cvt_f32_i32_e32 v69, v69
	v_cvt_f32_i32_e32 v50, v50
	v_cvt_f32_i32_e32 v54, v54
	v_cvt_f32_i32_e32 v62, v62
	v_cvt_f32_i32_e32 v58, v58
	v_cvt_f32_i32_e32 v55, v55
	v_cvt_f32_i32_e32 v51, v51
	v_cvt_f32_i32_e32 v59, v59
	v_cvt_f32_i32_e32 v63, v63
	v_cvt_f32_i32_e32 v56, v56
	s_waitcnt vmcnt(0)
	v_mul_f32_e32 v155, v155, v189
	v_mul_f32_e32 v154, v154, v189
	v_mul_f32_e32 v158, v158, v189
	v_mul_f32_e32 v147, v147, v189
	v_fma_f32 v155, v95, v155, v103
	v_mul_f32_e32 v155, 0xbfb8aa3b, v155
	v_fma_f32 v154, v94, v154, v102
	v_exp_f32_e32 v155, v155
	v_mul_f32_e32 v154, 0xbfb8aa3b, v154
	v_fma_f32 v158, v106, v158, v110
	v_fma_f32 v147, v83, v147, v91
	v_exp_f32_e32 v154, v154
	v_mul_f32_e32 v146, v146, v189
	v_mul_f32_e32 v158, 0xbfb8aa3b, v158
	v_mul_f32_e32 v147, 0xbfb8aa3b, v147
	v_fma_f32 v146, v82, v146, v90
	v_exp_f32_e32 v158, v158
	v_exp_f32_e32 v147, v147
	v_add_f32_e32 v155, 1.0, v155
	v_mul_f32_e32 v150, v150, v189
	v_mul_f32_e32 v146, 0xbfb8aa3b, v146
	v_rcp_f32_e32 v155, v155
	v_fma_f32 v150, v86, v150, v98
	v_exp_f32_e32 v146, v146
	v_add_f32_e32 v154, 1.0, v154
	v_mul_f32_e32 v150, 0xbfb8aa3b, v150
	v_rcp_f32_e32 v154, v154
	v_exp_f32_e32 v150, v150
	v_add_f32_e32 v158, 1.0, v158
	v_add_f32_e32 v147, 1.0, v147
	v_mul_f32_e32 v160, v160, v189
	v_rcp_f32_e32 v158, v158
	v_rcp_f32_e32 v195, v147
	v_mul_f32_e32 v197, v147, v155
	v_mul_f32_e32 v147, v156, v189
	v_fma_f32 v160, v108, v160, v112
	v_add_f32_e32 v146, 1.0, v146
	v_fma_f32 v147, v96, v147, v104
	v_rcp_f32_e32 v193, v146
	v_mul_f32_e32 v196, v146, v154
	v_mul_f32_e32 v146, 0xbfb8aa3b, v160
	v_mul_f32_e32 v147, 0xbfb8aa3b, v147
	v_add_f32_e32 v150, 1.0, v150
	v_exp_f32_e32 v146, v146
	v_exp_f32_e32 v147, v147
	v_rcp_f32_e32 v192, v150
	v_mul_f32_e32 v158, v150, v158
	v_mul_f32_e32 v150, v152, v189
	v_mul_f32_e32 v148, v148, v189
	v_fma_f32 v150, v88, v150, v100
	v_fma_f32 v148, v84, v148, v92
	v_mul_f32_e32 v150, 0xbfb8aa3b, v150
	v_mul_f32_e32 v148, 0xbfb8aa3b, v148
	v_exp_f32_e32 v150, v150
	v_exp_f32_e32 v148, v148
	v_add_f32_e32 v146, 1.0, v146
	v_add_f32_e32 v147, 1.0, v147
	v_rcp_f32_e32 v146, v146
	v_rcp_f32_e32 v147, v147
	v_mul_f32_e32 v159, v159, v189
	v_add_f32_e32 v150, 1.0, v150
	v_add_f32_e32 v148, 1.0, v148
	v_fma_f32 v159, v107, v159, v111
	v_mul_f32_e32 v156, v150, v146
	v_mul_f32_e32 v160, v148, v147
	v_mul_f32_e32 v146, v161, v189
	v_mul_f32_e32 v147, v157, v189
	v_mul_f32_e32 v159, 0xbfb8aa3b, v159
	v_fma_f32 v146, v109, v146, v113
	v_fma_f32 v147, v97, v147, v105
	v_exp_f32_e32 v159, v159
	v_mul_f32_e32 v146, 0xbfb8aa3b, v146
	v_mul_f32_e32 v147, 0xbfb8aa3b, v147
	v_mul_f32_e32 v151, v151, v189
	v_rcp_f32_e32 v152, v148
	v_exp_f32_e32 v146, v146
	v_exp_f32_e32 v147, v147
	v_mul_f32_e32 v148, v153, v189
	v_mul_f32_e32 v149, v149, v189
	v_fma_f32 v151, v87, v151, v99
	v_fma_f32 v148, v89, v148, v101
	v_fma_f32 v149, v85, v149, v93
	v_mul_f32_e32 v151, 0xbfb8aa3b, v151
	v_mul_f32_e32 v148, 0xbfb8aa3b, v148
	v_mul_f32_e32 v149, 0xbfb8aa3b, v149
	v_exp_f32_e32 v151, v151
	v_add_f32_e32 v159, 1.0, v159
	v_exp_f32_e32 v148, v148
	v_exp_f32_e32 v149, v149
	v_rcp_f32_e32 v159, v159
	v_add_f32_e32 v146, 1.0, v146
	v_add_f32_e32 v147, 1.0, v147
	v_rcp_f32_e32 v146, v146
	v_rcp_f32_e32 v147, v147
	v_add_f32_e32 v151, 1.0, v151
	v_add_f32_e32 v148, 1.0, v148
	v_add_f32_e32 v149, 1.0, v149
	v_rcp_f32_e32 v194, v151
	v_mul_f32_e32 v159, v151, v159
	v_rcp_f32_e32 v151, v150
	v_rcp_f32_e32 v150, v148
	v_rcp_f32_e32 v153, v149
	v_mul_f32_e32 v157, v148, v146
	v_mul_f32_e32 v161, v149, v147
	v_cvt_pk_bf16_f32 v148, v192, v194
	v_cvt_pk_bf16_f32 v149, v151, v150
	v_cvt_pk_bf16_f32 v150, v193, v195
	v_cvt_pk_bf16_f32 v151, v152, v153
	v_lshlrev_b64 v[152:153], 12, v[182:183]
	v_lshl_add_u64 v[154:155], s[16:17], 0, v[152:153]
	v_lshlrev_b64 v[146:147], 1, v[190:191]
	v_lshl_add_u64 v[154:155], v[154:155], 0, v[146:147]
	v_lshl_add_u64 v[152:153], s[10:11], 0, v[152:153]
	global_store_dwordx4 v[154:155], v[148:151], off
	v_lshl_add_u64 v[152:153], v[152:153], 0, v[146:147]
	v_cvt_f32_i32_e32 v52, v52
	v_cvt_pk_bf16_f32 v148, v158, v159
	v_cvt_pk_bf16_f32 v149, v156, v157
	v_cvt_pk_bf16_f32 v150, v196, v197
	v_cvt_pk_bf16_f32 v151, v160, v161
	global_store_dwordx4 v[152:153], v[148:151], off
	v_cvt_f32_i32_e32 v60, v60
	v_cvt_f32_i32_e32 v64, v64
	v_add_u32_e32 v148, 16, v182
	v_ashrrev_i32_e32 v149, 31, v148
	v_lshl_add_u64 v[150:151], v[148:149], 2, s[12:13]
	v_mov_b32_e32 v150, v198
	s_nop 0
	v_cvt_f32_i32_e32 v57, v57
	v_cvt_f32_i32_e32 v53, v53
	v_cvt_f32_i32_e32 v61, v61
	v_cvt_f32_i32_e32 v65, v65
	v_cvt_f32_i32_e32 v34, v34
	v_cvt_f32_i32_e32 v38, v38
	v_cvt_f32_i32_e32 v46, v46
	v_cvt_f32_i32_e32 v42, v42
	v_cvt_f32_i32_e32 v39, v39
	v_cvt_f32_i32_e32 v35, v35
	v_cvt_f32_i32_e32 v43, v43
	v_cvt_f32_i32_e32 v47, v47
	v_cvt_f32_i32_e32 v40, v40
	v_cvt_f32_i32_e32 v36, v36
	v_cvt_f32_i32_e32 v44, v44
	v_cvt_f32_i32_e32 v48, v48
	v_cvt_f32_i32_e32 v41, v41
	v_cvt_f32_i32_e32 v37, v37
	v_cvt_f32_i32_e32 v45, v45
	v_cvt_f32_i32_e32 v49, v49
	v_cvt_f32_i32_e32 v18, v18
	v_cvt_f32_i32_e32 v22, v22
	v_cvt_f32_i32_e32 v30, v30
	v_cvt_f32_i32_e32 v26, v26
	v_cvt_f32_i32_e32 v23, v23
	v_cvt_f32_i32_e32 v19, v19
	v_cvt_f32_i32_e32 v27, v27
	v_cvt_f32_i32_e32 v31, v31
	v_cvt_f32_i32_e32 v24, v24
	v_cvt_f32_i32_e32 v20, v20
	v_cvt_f32_i32_e32 v28, v28
	v_cvt_f32_i32_e32 v32, v32
	v_cvt_f32_i32_e32 v25, v25
	v_cvt_f32_i32_e32 v21, v21
	v_cvt_f32_i32_e32 v29, v29
	v_cvt_f32_i32_e32 v33, v33
	v_cvt_f32_i32_e32 v2, v2
	v_cvt_f32_i32_e32 v6, v6
	v_cvt_f32_i32_e32 v14, v14
	v_cvt_f32_i32_e32 v10, v10
	v_cvt_f32_i32_e32 v7, v7
	v_cvt_f32_i32_e32 v3, v3
	v_cvt_f32_i32_e32 v11, v11
	v_cvt_f32_i32_e32 v15, v15
	v_cvt_f32_i32_e32 v8, v8
	v_cvt_f32_i32_e32 v4, v4
	v_cvt_f32_i32_e32 v12, v12
	v_cvt_f32_i32_e32 v16, v16
	v_cvt_f32_i32_e32 v9, v9
	v_cvt_f32_i32_e32 v5, v5
	v_cvt_f32_i32_e32 v13, v13
	v_cvt_f32_i32_e32 v17, v17
	s_andn2_b64 vcc, exec, s[6:7]
	s_mov_b64 s[6:7], -1
	s_nop 0
	v_mul_f32_e32 v142, v142, v150
	v_mul_f32_e32 v138, v138, v150
	v_fma_f32 v142, v106, v142, v110
	v_fma_f32 v138, v94, v138, v102
	v_mul_f32_e32 v142, 0xbfb8aa3b, v142
	v_mul_f32_e32 v138, 0xbfb8aa3b, v138
	v_exp_f32_e32 v142, v142
	v_exp_f32_e32 v138, v138
	v_mul_f32_e32 v134, v134, v150
	v_mul_f32_e32 v130, v130, v150
	v_fma_f32 v134, v86, v134, v98
	v_fma_f32 v130, v82, v130, v90
	v_mul_f32_e32 v134, 0xbfb8aa3b, v134
	v_mul_f32_e32 v130, 0xbfb8aa3b, v130
	v_exp_f32_e32 v134, v134
	v_exp_f32_e32 v130, v130
	v_add_f32_e32 v142, 1.0, v142
	v_add_f32_e32 v138, 1.0, v138
	v_rcp_f32_e32 v142, v142
	v_rcp_f32_e32 v138, v138
	v_add_f32_e32 v134, 1.0, v134
	v_add_f32_e32 v130, 1.0, v130
	v_rcp_f32_e32 v151, v134
	v_rcp_f32_e32 v152, v130
	v_mul_f32_e32 v142, v134, v142
	v_mul_f32_e32 v138, v130, v138
	v_mul_f32_e32 v130, v143, v150
	v_mul_f32_e32 v134, v139, v150
	v_fma_f32 v130, v107, v130, v111
	v_fma_f32 v134, v95, v134, v103
	v_mul_f32_e32 v130, 0xbfb8aa3b, v130
	v_mul_f32_e32 v134, 0xbfb8aa3b, v134
	v_exp_f32_e32 v130, v130
	v_exp_f32_e32 v134, v134
	v_mul_f32_e32 v135, v135, v150
	v_mul_f32_e32 v131, v131, v150
	v_fma_f32 v135, v87, v135, v99
	v_fma_f32 v131, v83, v131, v91
	v_mul_f32_e32 v135, 0xbfb8aa3b, v135
	v_mul_f32_e32 v131, 0xbfb8aa3b, v131
	v_exp_f32_e32 v135, v135
	v_exp_f32_e32 v131, v131
	v_add_f32_e32 v130, 1.0, v130
	v_add_f32_e32 v134, 1.0, v134
	v_rcp_f32_e32 v130, v130
	v_rcp_f32_e32 v134, v134
	v_add_f32_e32 v135, 1.0, v135
	v_add_f32_e32 v131, 1.0, v131
	v_rcp_f32_e32 v143, v131
	v_mul_f32_e32 v153, v135, v130
	v_mul_f32_e32 v154, v131, v134
	v_mul_f32_e32 v130, v144, v150
	v_mul_f32_e32 v131, v140, v150
	v_fma_f32 v130, v108, v130, v112
	v_fma_f32 v131, v96, v131, v104
	v_mul_f32_e32 v130, 0xbfb8aa3b, v130
	v_mul_f32_e32 v131, 0xbfb8aa3b, v131
	v_exp_f32_e32 v130, v130
	v_exp_f32_e32 v131, v131
	v_mul_f32_e32 v134, v136, v150
	v_mul_f32_e32 v132, v132, v150
	v_fma_f32 v134, v88, v134, v100
	v_fma_f32 v132, v84, v132, v92
	v_mul_f32_e32 v134, 0xbfb8aa3b, v134
	v_mul_f32_e32 v132, 0xbfb8aa3b, v132
	v_exp_f32_e32 v134, v134
	v_exp_f32_e32 v132, v132
	v_add_f32_e32 v130, 1.0, v130
	v_add_f32_e32 v131, 1.0, v131
	v_rcp_f32_e32 v130, v130
	v_rcp_f32_e32 v131, v131
	v_add_f32_e32 v134, 1.0, v134
	v_add_f32_e32 v132, 1.0, v132
	v_mul_f32_e32 v140, v134, v130
	v_mul_f32_e32 v144, v132, v131
	v_mul_f32_e32 v130, v145, v150
	v_mul_f32_e32 v131, v141, v150
	v_fma_f32 v130, v109, v130, v113
	v_fma_f32 v131, v97, v131, v105
	v_mul_f32_e32 v130, 0xbfb8aa3b, v130
	v_mul_f32_e32 v131, 0xbfb8aa3b, v131
	v_rcp_f32_e32 v136, v132
	v_exp_f32_e32 v130, v130
	v_exp_f32_e32 v131, v131
	v_mul_f32_e32 v132, v137, v150
	v_fma_f32 v132, v89, v132, v101
	v_mul_f32_e32 v133, v133, v150
	v_mul_f32_e32 v132, 0xbfb8aa3b, v132
	v_fma_f32 v133, v85, v133, v93
	v_exp_f32_e32 v132, v132
	v_mul_f32_e32 v133, 0xbfb8aa3b, v133
	v_exp_f32_e32 v133, v133
	v_add_f32_e32 v130, 1.0, v130
	v_add_f32_e32 v131, 1.0, v131
	v_rcp_f32_e32 v130, v130
	v_rcp_f32_e32 v131, v131
	v_add_f32_e32 v132, 1.0, v132
	v_rcp_f32_e32 v139, v135
	v_rcp_f32_e32 v135, v134
	v_add_f32_e32 v133, 1.0, v133
	v_rcp_f32_e32 v134, v132
	v_rcp_f32_e32 v137, v133
	v_mul_f32_e32 v141, v132, v130
	v_mul_f32_e32 v145, v133, v131
	v_cvt_pk_bf16_f32 v130, v151, v139
	v_cvt_pk_bf16_f32 v131, v135, v134
	v_lshlrev_b64 v[134:135], 12, v[148:149]
	v_cvt_pk_bf16_f32 v132, v152, v143
	v_cvt_pk_bf16_f32 v133, v136, v137
	v_lshl_add_u64 v[136:137], s[16:17], 0, v[134:135]
	v_lshl_add_u64 v[136:137], v[136:137], 0, v[146:147]
	v_lshl_add_u64 v[134:135], s[10:11], 0, v[134:135]
	global_store_dwordx4 v[136:137], v[130:133], off
	v_lshl_add_u64 v[134:135], v[134:135], 0, v[146:147]
	s_nop 0
	v_cvt_pk_bf16_f32 v130, v142, v153
	v_cvt_pk_bf16_f32 v131, v140, v141
	v_cvt_pk_bf16_f32 v132, v138, v154
	v_cvt_pk_bf16_f32 v133, v144, v145
	global_store_dwordx4 v[134:135], v[130:133], off
	s_nop 1
	v_add_u32_e32 v130, 32, v182
	v_ashrrev_i32_e32 v131, 31, v130
	v_lshl_add_u64 v[132:133], v[130:131], 2, s[12:13]
	v_mov_b32_e32 v132, v199
	v_mul_f32_e32 v126, v126, v132
	v_mul_f32_e32 v122, v122, v132
	v_fma_f32 v126, v106, v126, v110
	v_fma_f32 v122, v94, v122, v102
	v_mul_f32_e32 v126, 0xbfb8aa3b, v126
	v_mul_f32_e32 v122, 0xbfb8aa3b, v122
	v_exp_f32_e32 v126, v126
	v_exp_f32_e32 v122, v122
	v_mul_f32_e32 v118, v118, v132
	v_mul_f32_e32 v114, v114, v132
	v_fma_f32 v118, v86, v118, v98
	v_fma_f32 v114, v82, v114, v90
	v_mul_f32_e32 v118, 0xbfb8aa3b, v118
	v_mul_f32_e32 v114, 0xbfb8aa3b, v114
	v_exp_f32_e32 v118, v118
	v_exp_f32_e32 v114, v114
	v_add_f32_e32 v126, 1.0, v126
	v_add_f32_e32 v122, 1.0, v122
	v_rcp_f32_e32 v126, v126
	v_rcp_f32_e32 v122, v122
	v_add_f32_e32 v118, 1.0, v118
	v_add_f32_e32 v114, 1.0, v114
	v_rcp_f32_e32 v133, v118
	v_rcp_f32_e32 v134, v114
	v_mul_f32_e32 v126, v118, v126
	v_mul_f32_e32 v122, v114, v122
	v_mul_f32_e32 v114, v127, v132
	v_mul_f32_e32 v118, v123, v132
	v_fma_f32 v114, v107, v114, v111
	v_fma_f32 v118, v95, v118, v103
	v_mul_f32_e32 v114, 0xbfb8aa3b, v114
	v_mul_f32_e32 v118, 0xbfb8aa3b, v118
	v_exp_f32_e32 v114, v114
	v_exp_f32_e32 v118, v118
	v_mul_f32_e32 v119, v119, v132
	v_mul_f32_e32 v115, v115, v132
	v_fma_f32 v119, v87, v119, v99
	v_fma_f32 v115, v83, v115, v91
	v_mul_f32_e32 v119, 0xbfb8aa3b, v119
	v_mul_f32_e32 v115, 0xbfb8aa3b, v115
	v_exp_f32_e32 v119, v119
	v_exp_f32_e32 v115, v115
	v_add_f32_e32 v114, 1.0, v114
	v_add_f32_e32 v118, 1.0, v118
	v_rcp_f32_e32 v114, v114
	v_rcp_f32_e32 v118, v118
	v_add_f32_e32 v119, 1.0, v119
	v_add_f32_e32 v115, 1.0, v115
	v_rcp_f32_e32 v127, v115
	v_mul_f32_e32 v135, v119, v114
	v_mul_f32_e32 v136, v115, v118
	v_mul_f32_e32 v114, v128, v132
	v_mul_f32_e32 v115, v124, v132
	v_fma_f32 v114, v108, v114, v112
	v_fma_f32 v115, v96, v115, v104
	v_mul_f32_e32 v114, 0xbfb8aa3b, v114
	v_mul_f32_e32 v115, 0xbfb8aa3b, v115
	v_exp_f32_e32 v114, v114
	v_exp_f32_e32 v115, v115
	v_mul_f32_e32 v118, v120, v132
	v_mul_f32_e32 v116, v116, v132
	v_fma_f32 v118, v88, v118, v100
	v_fma_f32 v116, v84, v116, v92
	v_mul_f32_e32 v118, 0xbfb8aa3b, v118
	v_mul_f32_e32 v116, 0xbfb8aa3b, v116
	v_exp_f32_e32 v118, v118
	v_exp_f32_e32 v116, v116
	v_add_f32_e32 v114, 1.0, v114
	v_add_f32_e32 v115, 1.0, v115
	v_rcp_f32_e32 v114, v114
	v_rcp_f32_e32 v115, v115
	v_add_f32_e32 v118, 1.0, v118
	v_add_f32_e32 v116, 1.0, v116
	v_mul_f32_e32 v124, v118, v114
	v_mul_f32_e32 v128, v116, v115
	v_mul_f32_e32 v114, v129, v132
	v_mul_f32_e32 v115, v125, v132
	v_fma_f32 v114, v109, v114, v113
	v_fma_f32 v115, v97, v115, v105
	v_mul_f32_e32 v114, 0xbfb8aa3b, v114
	v_mul_f32_e32 v115, 0xbfb8aa3b, v115
	v_rcp_f32_e32 v120, v116
	v_exp_f32_e32 v114, v114
	v_exp_f32_e32 v115, v115
	v_mul_f32_e32 v116, v121, v132
	v_fma_f32 v116, v89, v116, v101
	v_mul_f32_e32 v117, v117, v132
	v_mul_f32_e32 v116, 0xbfb8aa3b, v116
	v_fma_f32 v117, v85, v117, v93
	v_exp_f32_e32 v116, v116
	v_mul_f32_e32 v117, 0xbfb8aa3b, v117
	v_exp_f32_e32 v117, v117
	v_add_f32_e32 v114, 1.0, v114
	v_add_f32_e32 v115, 1.0, v115
	v_rcp_f32_e32 v114, v114
	v_rcp_f32_e32 v115, v115
	v_add_f32_e32 v116, 1.0, v116
	v_rcp_f32_e32 v123, v119
	v_rcp_f32_e32 v119, v118
	v_add_f32_e32 v117, 1.0, v117
	v_rcp_f32_e32 v118, v116
	v_rcp_f32_e32 v121, v117
	v_mul_f32_e32 v125, v116, v114
	v_mul_f32_e32 v129, v117, v115
	v_cvt_pk_bf16_f32 v114, v133, v123
	v_cvt_pk_bf16_f32 v115, v119, v118
	v_lshlrev_b64 v[118:119], 12, v[130:131]
	v_cvt_pk_bf16_f32 v116, v134, v127
	v_cvt_pk_bf16_f32 v117, v120, v121
	v_lshl_add_u64 v[120:121], s[16:17], 0, v[118:119]
	v_lshl_add_u64 v[120:121], v[120:121], 0, v[146:147]
	v_lshl_add_u64 v[118:119], s[10:11], 0, v[118:119]
	global_store_dwordx4 v[120:121], v[114:117], off
	v_lshl_add_u64 v[118:119], v[118:119], 0, v[146:147]
	s_nop 0
	v_cvt_pk_bf16_f32 v114, v126, v135
	v_cvt_pk_bf16_f32 v115, v124, v125
	v_cvt_pk_bf16_f32 v116, v122, v136
	v_cvt_pk_bf16_f32 v117, v128, v129
	global_store_dwordx4 v[118:119], v[114:117], off
	s_nop 1
	v_add_u32_e32 v114, 48, v182
	v_ashrrev_i32_e32 v115, 31, v114
	v_lshl_add_u64 v[116:117], v[114:115], 2, s[12:13]
	v_mov_b32_e32 v116, v200
	v_mul_f32_e32 v78, v78, v116
	v_mul_f32_e32 v74, v74, v116
	v_fma_f32 v78, v106, v78, v110
	v_fma_f32 v74, v94, v74, v102
	v_mul_f32_e32 v78, 0xbfb8aa3b, v78
	v_mul_f32_e32 v74, 0xbfb8aa3b, v74
	v_exp_f32_e32 v78, v78
	v_exp_f32_e32 v74, v74
	v_mul_f32_e32 v70, v70, v116
	v_mul_f32_e32 v66, v66, v116
	v_fma_f32 v70, v86, v70, v98
	v_fma_f32 v66, v82, v66, v90
	v_mul_f32_e32 v70, 0xbfb8aa3b, v70
	v_mul_f32_e32 v66, 0xbfb8aa3b, v66
	v_exp_f32_e32 v70, v70
	v_exp_f32_e32 v66, v66
	v_add_f32_e32 v78, 1.0, v78
	v_add_f32_e32 v74, 1.0, v74
	v_rcp_f32_e32 v78, v78
	v_rcp_f32_e32 v74, v74
	v_add_f32_e32 v70, 1.0, v70
	v_add_f32_e32 v66, 1.0, v66
	v_rcp_f32_e32 v117, v70
	v_rcp_f32_e32 v118, v66
	v_mul_f32_e32 v78, v70, v78
	v_mul_f32_e32 v74, v66, v74
	v_mul_f32_e32 v66, v79, v116
	v_mul_f32_e32 v70, v75, v116
	v_fma_f32 v66, v107, v66, v111
	v_fma_f32 v70, v95, v70, v103
	v_mul_f32_e32 v66, 0xbfb8aa3b, v66
	v_mul_f32_e32 v70, 0xbfb8aa3b, v70
	v_exp_f32_e32 v66, v66
	v_exp_f32_e32 v70, v70
	v_mul_f32_e32 v71, v71, v116
	v_mul_f32_e32 v67, v67, v116
	v_fma_f32 v71, v87, v71, v99
	v_fma_f32 v67, v83, v67, v91
	v_mul_f32_e32 v71, 0xbfb8aa3b, v71
	v_mul_f32_e32 v67, 0xbfb8aa3b, v67
	v_exp_f32_e32 v71, v71
	v_exp_f32_e32 v67, v67
	v_add_f32_e32 v66, 1.0, v66
	v_add_f32_e32 v70, 1.0, v70
	v_rcp_f32_e32 v66, v66
	v_rcp_f32_e32 v70, v70
	v_add_f32_e32 v71, 1.0, v71
	v_add_f32_e32 v67, 1.0, v67
	v_rcp_f32_e32 v79, v67
	v_mul_f32_e32 v119, v71, v66
	v_mul_f32_e32 v120, v67, v70
	v_mul_f32_e32 v66, v80, v116
	v_mul_f32_e32 v67, v76, v116
	v_fma_f32 v66, v108, v66, v112
	v_fma_f32 v67, v96, v67, v104
	v_mul_f32_e32 v66, 0xbfb8aa3b, v66
	v_mul_f32_e32 v67, 0xbfb8aa3b, v67
	v_exp_f32_e32 v66, v66
	v_exp_f32_e32 v67, v67
	v_mul_f32_e32 v70, v72, v116
	v_mul_f32_e32 v68, v68, v116
	v_fma_f32 v70, v88, v70, v100
	v_fma_f32 v68, v84, v68, v92
	v_mul_f32_e32 v70, 0xbfb8aa3b, v70
	v_mul_f32_e32 v68, 0xbfb8aa3b, v68
	v_exp_f32_e32 v70, v70
	v_exp_f32_e32 v68, v68
	v_add_f32_e32 v66, 1.0, v66
	v_add_f32_e32 v67, 1.0, v67
	v_rcp_f32_e32 v66, v66
	v_rcp_f32_e32 v67, v67
	v_add_f32_e32 v70, 1.0, v70
	v_add_f32_e32 v68, 1.0, v68
	v_mul_f32_e32 v76, v70, v66
	v_mul_f32_e32 v80, v68, v67
	v_mul_f32_e32 v66, v81, v116
	v_mul_f32_e32 v67, v77, v116
	v_fma_f32 v66, v109, v66, v113
	v_fma_f32 v67, v97, v67, v105
	v_mul_f32_e32 v66, 0xbfb8aa3b, v66
	v_mul_f32_e32 v67, 0xbfb8aa3b, v67
	v_rcp_f32_e32 v72, v68
	v_exp_f32_e32 v66, v66
	v_exp_f32_e32 v67, v67
	v_mul_f32_e32 v68, v73, v116
	v_fma_f32 v68, v89, v68, v101
	v_mul_f32_e32 v69, v69, v116
	v_mul_f32_e32 v68, 0xbfb8aa3b, v68
	v_fma_f32 v69, v85, v69, v93
	v_exp_f32_e32 v68, v68
	v_mul_f32_e32 v69, 0xbfb8aa3b, v69
	v_exp_f32_e32 v69, v69
	v_add_f32_e32 v66, 1.0, v66
	v_add_f32_e32 v67, 1.0, v67
	v_rcp_f32_e32 v66, v66
	v_rcp_f32_e32 v67, v67
	v_add_f32_e32 v68, 1.0, v68
	v_rcp_f32_e32 v75, v71
	v_rcp_f32_e32 v71, v70
	v_add_f32_e32 v69, 1.0, v69
	v_rcp_f32_e32 v70, v68
	v_rcp_f32_e32 v73, v69
	v_mul_f32_e32 v77, v68, v66
	v_mul_f32_e32 v81, v69, v67
	v_cvt_pk_bf16_f32 v66, v117, v75
	v_cvt_pk_bf16_f32 v67, v71, v70
	v_lshlrev_b64 v[70:71], 12, v[114:115]
	v_cvt_pk_bf16_f32 v68, v118, v79
	v_cvt_pk_bf16_f32 v69, v72, v73
	v_lshl_add_u64 v[72:73], s[16:17], 0, v[70:71]
	v_lshl_add_u64 v[72:73], v[72:73], 0, v[146:147]
	v_lshl_add_u64 v[70:71], s[10:11], 0, v[70:71]
	global_store_dwordx4 v[72:73], v[66:69], off
	v_lshl_add_u64 v[70:71], v[70:71], 0, v[146:147]
	s_nop 0
	v_cvt_pk_bf16_f32 v66, v78, v119
	v_cvt_pk_bf16_f32 v67, v76, v77
	v_cvt_pk_bf16_f32 v68, v74, v120
	v_cvt_pk_bf16_f32 v69, v80, v81
	global_store_dwordx4 v[70:71], v[66:69], off
	s_nop 1
	v_add_u32_e32 v66, 0x80, v182
	v_ashrrev_i32_e32 v67, 31, v66
	v_lshl_add_u64 v[68:69], v[66:67], 2, s[12:13]
	v_mov_b32_e32 v68, v201
	v_mul_f32_e32 v50, v50, v68
	v_fma_f32 v50, v94, v50, v102
	v_mul_f32_e32 v50, 0xbfb8aa3b, v50
	v_exp_f32_e32 v50, v50
	v_mul_f32_e32 v54, v54, v68
	v_mul_f32_e32 v62, v62, v68
	v_fma_f32 v54, v106, v54, v110
	v_fma_f32 v62, v82, v62, v90
	v_mul_f32_e32 v54, 0xbfb8aa3b, v54
	v_mul_f32_e32 v62, 0xbfb8aa3b, v62
	v_exp_f32_e32 v54, v54
	v_exp_f32_e32 v62, v62
	v_add_f32_e32 v50, 1.0, v50
	v_mul_f32_e32 v58, v58, v68
	v_rcp_f32_e32 v50, v50
	v_fma_f32 v58, v86, v58, v98
	v_mul_f32_e32 v58, 0xbfb8aa3b, v58
	v_exp_f32_e32 v58, v58
	v_add_f32_e32 v54, 1.0, v54
	v_add_f32_e32 v62, 1.0, v62
	v_rcp_f32_e32 v54, v54
	v_rcp_f32_e32 v70, v62
	v_mul_f32_e32 v62, v62, v50
	v_mul_f32_e32 v50, v55, v68
	v_mul_f32_e32 v51, v51, v68
	v_fma_f32 v50, v107, v50, v111
	v_fma_f32 v51, v95, v51, v103
	v_mul_f32_e32 v50, 0xbfb8aa3b, v50
	v_mul_f32_e32 v51, 0xbfb8aa3b, v51
	v_add_f32_e32 v58, 1.0, v58
	v_exp_f32_e32 v50, v50
	v_exp_f32_e32 v51, v51
	v_rcp_f32_e32 v69, v58
	v_mul_f32_e32 v58, v58, v54
	v_mul_f32_e32 v54, v59, v68
	v_mul_f32_e32 v55, v63, v68
	v_fma_f32 v54, v87, v54, v99
	v_fma_f32 v55, v83, v55, v91
	v_mul_f32_e32 v54, 0xbfb8aa3b, v54
	v_mul_f32_e32 v55, 0xbfb8aa3b, v55
	v_exp_f32_e32 v54, v54
	v_exp_f32_e32 v55, v55
	v_add_f32_e32 v50, 1.0, v50
	v_add_f32_e32 v51, 1.0, v51
	v_rcp_f32_e32 v50, v50
	v_rcp_f32_e32 v51, v51
	v_add_f32_e32 v54, 1.0, v54
	v_add_f32_e32 v55, 1.0, v55
	v_mul_f32_e32 v71, v54, v50
	v_mul_f32_e32 v72, v55, v51
	v_mul_f32_e32 v50, v56, v68
	v_mul_f32_e32 v51, v52, v68
	v_fma_f32 v50, v108, v50, v112
	v_fma_f32 v51, v96, v51, v104
	v_mul_f32_e32 v50, 0xbfb8aa3b, v50
	v_mul_f32_e32 v51, 0xbfb8aa3b, v51
	v_exp_f32_e32 v50, v50
	v_exp_f32_e32 v51, v51
	v_rcp_f32_e32 v59, v54
	v_mul_f32_e32 v52, v60, v68
	v_mul_f32_e32 v54, v64, v68
	v_fma_f32 v52, v88, v52, v100
	v_fma_f32 v54, v84, v54, v92
	v_mul_f32_e32 v52, 0xbfb8aa3b, v52
	v_mul_f32_e32 v54, 0xbfb8aa3b, v54
	v_exp_f32_e32 v52, v52
	v_exp_f32_e32 v54, v54
	v_add_f32_e32 v50, 1.0, v50
	v_add_f32_e32 v51, 1.0, v51
	v_rcp_f32_e32 v50, v50
	v_rcp_f32_e32 v51, v51
	v_add_f32_e32 v52, 1.0, v52
	v_add_f32_e32 v54, 1.0, v54
	v_mul_f32_e32 v60, v52, v50
	v_mul_f32_e32 v64, v54, v51
	v_mul_f32_e32 v50, v57, v68
	v_mul_f32_e32 v51, v53, v68
	v_fma_f32 v50, v109, v50, v113
	v_fma_f32 v51, v97, v51, v105
	v_mul_f32_e32 v50, 0xbfb8aa3b, v50
	v_mul_f32_e32 v51, 0xbfb8aa3b, v51
	v_rcp_f32_e32 v63, v55
	v_rcp_f32_e32 v55, v52
	v_exp_f32_e32 v50, v50
	v_exp_f32_e32 v51, v51
	v_mul_f32_e32 v52, v61, v68
	v_fma_f32 v52, v89, v52, v101
	v_mul_f32_e32 v53, v65, v68
	v_mul_f32_e32 v52, 0xbfb8aa3b, v52
	v_fma_f32 v53, v85, v53, v93
	v_exp_f32_e32 v52, v52
	v_mul_f32_e32 v53, 0xbfb8aa3b, v53
	v_exp_f32_e32 v53, v53
	v_add_f32_e32 v50, 1.0, v50
	v_add_f32_e32 v51, 1.0, v51
	v_rcp_f32_e32 v50, v50
	v_rcp_f32_e32 v51, v51
	v_add_f32_e32 v52, 1.0, v52
	v_rcp_f32_e32 v56, v54
	v_add_f32_e32 v53, 1.0, v53
	v_rcp_f32_e32 v54, v52
	v_rcp_f32_e32 v57, v53
	v_mul_f32_e32 v61, v52, v50
	v_mul_f32_e32 v65, v53, v51
	v_cvt_pk_bf16_f32 v50, v69, v59
	v_cvt_pk_bf16_f32 v51, v55, v54
	v_lshlrev_b64 v[54:55], 12, v[66:67]
	v_cvt_pk_bf16_f32 v52, v70, v63
	v_cvt_pk_bf16_f32 v53, v56, v57
	v_lshl_add_u64 v[56:57], s[16:17], 0, v[54:55]
	v_lshl_add_u64 v[56:57], v[56:57], 0, v[146:147]
	v_lshl_add_u64 v[54:55], s[10:11], 0, v[54:55]
	global_store_dwordx4 v[56:57], v[50:53], off
	v_lshl_add_u64 v[54:55], v[54:55], 0, v[146:147]
	s_nop 0
	v_cvt_pk_bf16_f32 v50, v58, v71
	v_cvt_pk_bf16_f32 v51, v60, v61
	v_cvt_pk_bf16_f32 v52, v62, v72
	v_cvt_pk_bf16_f32 v53, v64, v65
	global_store_dwordx4 v[54:55], v[50:53], off
	s_nop 1
	v_add_u32_e32 v50, 0x90, v182
	v_ashrrev_i32_e32 v51, 31, v50
	v_lshl_add_u64 v[52:53], v[50:51], 2, s[12:13]
	v_mov_b32_e32 v52, v202
	v_mul_f32_e32 v34, v34, v52
	v_fma_f32 v34, v94, v34, v102
	v_mul_f32_e32 v34, 0xbfb8aa3b, v34
	v_exp_f32_e32 v34, v34
	v_mul_f32_e32 v38, v38, v52
	v_mul_f32_e32 v46, v46, v52
	v_fma_f32 v38, v106, v38, v110
	v_fma_f32 v46, v82, v46, v90
	v_mul_f32_e32 v38, 0xbfb8aa3b, v38
	v_mul_f32_e32 v46, 0xbfb8aa3b, v46
	v_exp_f32_e32 v38, v38
	v_exp_f32_e32 v46, v46
	v_add_f32_e32 v34, 1.0, v34
	v_mul_f32_e32 v42, v42, v52
	v_rcp_f32_e32 v34, v34
	v_fma_f32 v42, v86, v42, v98
	v_mul_f32_e32 v42, 0xbfb8aa3b, v42
	v_exp_f32_e32 v42, v42
	v_add_f32_e32 v38, 1.0, v38
	v_add_f32_e32 v46, 1.0, v46
	v_rcp_f32_e32 v38, v38
	v_rcp_f32_e32 v54, v46
	v_mul_f32_e32 v46, v46, v34
	v_mul_f32_e32 v34, v39, v52
	v_mul_f32_e32 v35, v35, v52
	v_fma_f32 v34, v107, v34, v111
	v_fma_f32 v35, v95, v35, v103
	v_mul_f32_e32 v34, 0xbfb8aa3b, v34
	v_mul_f32_e32 v35, 0xbfb8aa3b, v35
	v_add_f32_e32 v42, 1.0, v42
	v_exp_f32_e32 v34, v34
	v_exp_f32_e32 v35, v35
	v_rcp_f32_e32 v53, v42
	v_mul_f32_e32 v42, v42, v38
	v_mul_f32_e32 v38, v43, v52
	v_mul_f32_e32 v39, v47, v52
	v_fma_f32 v38, v87, v38, v99
	v_fma_f32 v39, v83, v39, v91
	v_mul_f32_e32 v38, 0xbfb8aa3b, v38
	v_mul_f32_e32 v39, 0xbfb8aa3b, v39
	v_exp_f32_e32 v38, v38
	v_exp_f32_e32 v39, v39
	v_add_f32_e32 v34, 1.0, v34
	v_add_f32_e32 v35, 1.0, v35
	v_rcp_f32_e32 v34, v34
	v_rcp_f32_e32 v35, v35
	v_add_f32_e32 v38, 1.0, v38
	v_add_f32_e32 v39, 1.0, v39
	v_mul_f32_e32 v55, v38, v34
	v_mul_f32_e32 v56, v39, v35
	v_mul_f32_e32 v34, v40, v52
	v_mul_f32_e32 v35, v36, v52
	v_fma_f32 v34, v108, v34, v112
	v_fma_f32 v35, v96, v35, v104
	v_mul_f32_e32 v34, 0xbfb8aa3b, v34
	v_mul_f32_e32 v35, 0xbfb8aa3b, v35
	v_exp_f32_e32 v34, v34
	v_exp_f32_e32 v35, v35
	v_rcp_f32_e32 v43, v38
	v_mul_f32_e32 v36, v44, v52
	v_mul_f32_e32 v38, v48, v52
	v_fma_f32 v36, v88, v36, v100
	v_fma_f32 v38, v84, v38, v92
	v_mul_f32_e32 v36, 0xbfb8aa3b, v36
	v_mul_f32_e32 v38, 0xbfb8aa3b, v38
	v_exp_f32_e32 v36, v36
	v_exp_f32_e32 v38, v38
	v_add_f32_e32 v34, 1.0, v34
	v_add_f32_e32 v35, 1.0, v35
	v_rcp_f32_e32 v34, v34
	v_rcp_f32_e32 v35, v35
	v_add_f32_e32 v36, 1.0, v36
	v_add_f32_e32 v38, 1.0, v38
	v_mul_f32_e32 v44, v36, v34
	v_mul_f32_e32 v48, v38, v35
	v_mul_f32_e32 v34, v41, v52
	v_mul_f32_e32 v35, v37, v52
	v_fma_f32 v34, v109, v34, v113
	v_fma_f32 v35, v97, v35, v105
	v_mul_f32_e32 v34, 0xbfb8aa3b, v34
	v_mul_f32_e32 v35, 0xbfb8aa3b, v35
	v_rcp_f32_e32 v47, v39
	v_rcp_f32_e32 v39, v36
	v_exp_f32_e32 v34, v34
	v_exp_f32_e32 v35, v35
	v_mul_f32_e32 v36, v45, v52
	v_fma_f32 v36, v89, v36, v101
	v_mul_f32_e32 v37, v49, v52
	v_mul_f32_e32 v36, 0xbfb8aa3b, v36
	v_fma_f32 v37, v85, v37, v93
	v_exp_f32_e32 v36, v36
	v_mul_f32_e32 v37, 0xbfb8aa3b, v37
	v_exp_f32_e32 v37, v37
	v_add_f32_e32 v34, 1.0, v34
	v_add_f32_e32 v35, 1.0, v35
	v_rcp_f32_e32 v34, v34
	v_rcp_f32_e32 v35, v35
	v_add_f32_e32 v36, 1.0, v36
	v_rcp_f32_e32 v40, v38
	v_add_f32_e32 v37, 1.0, v37
	v_rcp_f32_e32 v38, v36
	v_rcp_f32_e32 v41, v37
	v_mul_f32_e32 v45, v36, v34
	v_mul_f32_e32 v49, v37, v35
	v_cvt_pk_bf16_f32 v34, v53, v43
	v_cvt_pk_bf16_f32 v35, v39, v38
	v_lshlrev_b64 v[38:39], 12, v[50:51]
	v_cvt_pk_bf16_f32 v36, v54, v47
	v_cvt_pk_bf16_f32 v37, v40, v41
	v_lshl_add_u64 v[40:41], s[16:17], 0, v[38:39]
	v_lshl_add_u64 v[40:41], v[40:41], 0, v[146:147]
	v_lshl_add_u64 v[38:39], s[10:11], 0, v[38:39]
	global_store_dwordx4 v[40:41], v[34:37], off
	v_lshl_add_u64 v[38:39], v[38:39], 0, v[146:147]
	s_nop 0
	v_cvt_pk_bf16_f32 v34, v42, v55
	v_cvt_pk_bf16_f32 v35, v44, v45
	v_cvt_pk_bf16_f32 v36, v46, v56
	v_cvt_pk_bf16_f32 v37, v48, v49
	global_store_dwordx4 v[38:39], v[34:37], off
	s_nop 1
	v_add_u32_e32 v34, 0xa0, v182
	v_ashrrev_i32_e32 v35, 31, v34
	v_lshl_add_u64 v[36:37], v[34:35], 2, s[12:13]
	v_mov_b32_e32 v36, v203
	v_mul_f32_e32 v18, v18, v36
	v_fma_f32 v18, v94, v18, v102
	v_mul_f32_e32 v18, 0xbfb8aa3b, v18
	v_exp_f32_e32 v18, v18
	v_mul_f32_e32 v22, v22, v36
	v_mul_f32_e32 v30, v30, v36
	v_fma_f32 v22, v106, v22, v110
	v_fma_f32 v30, v82, v30, v90
	v_mul_f32_e32 v22, 0xbfb8aa3b, v22
	v_mul_f32_e32 v30, 0xbfb8aa3b, v30
	v_exp_f32_e32 v22, v22
	v_exp_f32_e32 v30, v30
	v_add_f32_e32 v18, 1.0, v18
	v_mul_f32_e32 v26, v26, v36
	v_rcp_f32_e32 v18, v18
	v_fma_f32 v26, v86, v26, v98
	v_mul_f32_e32 v26, 0xbfb8aa3b, v26
	v_exp_f32_e32 v26, v26
	v_add_f32_e32 v22, 1.0, v22
	v_add_f32_e32 v30, 1.0, v30
	v_rcp_f32_e32 v22, v22
	v_rcp_f32_e32 v38, v30
	v_mul_f32_e32 v30, v30, v18
	v_mul_f32_e32 v18, v23, v36
	v_mul_f32_e32 v19, v19, v36
	v_fma_f32 v18, v107, v18, v111
	v_fma_f32 v19, v95, v19, v103
	v_mul_f32_e32 v18, 0xbfb8aa3b, v18
	v_mul_f32_e32 v19, 0xbfb8aa3b, v19
	v_add_f32_e32 v26, 1.0, v26
	v_exp_f32_e32 v18, v18
	v_exp_f32_e32 v19, v19
	v_rcp_f32_e32 v37, v26
	v_mul_f32_e32 v26, v26, v22
	v_mul_f32_e32 v22, v27, v36
	v_mul_f32_e32 v23, v31, v36
	v_fma_f32 v22, v87, v22, v99
	v_fma_f32 v23, v83, v23, v91
	v_mul_f32_e32 v22, 0xbfb8aa3b, v22
	v_mul_f32_e32 v23, 0xbfb8aa3b, v23
	v_exp_f32_e32 v22, v22
	v_exp_f32_e32 v23, v23
	v_add_f32_e32 v18, 1.0, v18
	v_add_f32_e32 v19, 1.0, v19
	v_rcp_f32_e32 v18, v18
	v_rcp_f32_e32 v19, v19
	v_add_f32_e32 v22, 1.0, v22
	v_add_f32_e32 v23, 1.0, v23
	v_mul_f32_e32 v39, v22, v18
	v_mul_f32_e32 v40, v23, v19
	v_mul_f32_e32 v18, v24, v36
	v_mul_f32_e32 v19, v20, v36
	v_fma_f32 v18, v108, v18, v112
	v_fma_f32 v19, v96, v19, v104
	v_mul_f32_e32 v18, 0xbfb8aa3b, v18
	v_mul_f32_e32 v19, 0xbfb8aa3b, v19
	v_exp_f32_e32 v18, v18
	v_exp_f32_e32 v19, v19
	v_rcp_f32_e32 v27, v22
	v_mul_f32_e32 v20, v28, v36
	v_mul_f32_e32 v22, v32, v36
	v_fma_f32 v20, v88, v20, v100
	v_fma_f32 v22, v84, v22, v92
	v_mul_f32_e32 v20, 0xbfb8aa3b, v20
	v_mul_f32_e32 v22, 0xbfb8aa3b, v22
	v_exp_f32_e32 v20, v20
	v_exp_f32_e32 v22, v22
	v_add_f32_e32 v18, 1.0, v18
	v_add_f32_e32 v19, 1.0, v19
	v_rcp_f32_e32 v18, v18
	v_rcp_f32_e32 v19, v19
	v_add_f32_e32 v20, 1.0, v20
	v_add_f32_e32 v22, 1.0, v22
	v_mul_f32_e32 v28, v20, v18
	v_mul_f32_e32 v32, v22, v19
	v_mul_f32_e32 v18, v25, v36
	v_mul_f32_e32 v19, v21, v36
	v_fma_f32 v18, v109, v18, v113
	v_fma_f32 v19, v97, v19, v105
	v_mul_f32_e32 v18, 0xbfb8aa3b, v18
	v_mul_f32_e32 v19, 0xbfb8aa3b, v19
	v_rcp_f32_e32 v31, v23
	v_rcp_f32_e32 v23, v20
	v_exp_f32_e32 v18, v18
	v_exp_f32_e32 v19, v19
	v_mul_f32_e32 v20, v29, v36
	v_fma_f32 v20, v89, v20, v101
	v_mul_f32_e32 v21, v33, v36
	v_mul_f32_e32 v20, 0xbfb8aa3b, v20
	v_fma_f32 v21, v85, v21, v93
	v_exp_f32_e32 v20, v20
	v_mul_f32_e32 v21, 0xbfb8aa3b, v21
	v_exp_f32_e32 v21, v21
	v_add_f32_e32 v18, 1.0, v18
	v_add_f32_e32 v19, 1.0, v19
	v_rcp_f32_e32 v18, v18
	v_rcp_f32_e32 v19, v19
	v_add_f32_e32 v20, 1.0, v20
	v_rcp_f32_e32 v24, v22
	v_add_f32_e32 v21, 1.0, v21
	v_rcp_f32_e32 v22, v20
	v_rcp_f32_e32 v25, v21
	v_mul_f32_e32 v29, v20, v18
	v_mul_f32_e32 v33, v21, v19
	v_cvt_pk_bf16_f32 v18, v37, v27
	v_cvt_pk_bf16_f32 v19, v23, v22
	v_lshlrev_b64 v[22:23], 12, v[34:35]
	v_cvt_pk_bf16_f32 v20, v38, v31
	v_cvt_pk_bf16_f32 v21, v24, v25
	v_lshl_add_u64 v[24:25], s[16:17], 0, v[22:23]
	v_lshl_add_u64 v[24:25], v[24:25], 0, v[146:147]
	v_lshl_add_u64 v[22:23], s[10:11], 0, v[22:23]
	global_store_dwordx4 v[24:25], v[18:21], off
	v_lshl_add_u64 v[22:23], v[22:23], 0, v[146:147]
	s_nop 0
	v_cvt_pk_bf16_f32 v18, v26, v39
	v_cvt_pk_bf16_f32 v19, v28, v29
	v_cvt_pk_bf16_f32 v20, v30, v40
	v_cvt_pk_bf16_f32 v21, v32, v33
	global_store_dwordx4 v[22:23], v[18:21], off
	s_nop 1
	v_add_u32_e32 v18, 0xb0, v182
	v_ashrrev_i32_e32 v19, 31, v18
	v_lshl_add_u64 v[20:21], v[18:19], 2, s[12:13]
	v_mov_b32_e32 v20, v204
	v_mul_f32_e32 v2, v2, v20
	v_fma_f32 v2, v94, v2, v102
	v_mul_f32_e32 v2, 0xbfb8aa3b, v2
	v_exp_f32_e32 v2, v2
	v_mul_f32_e32 v6, v6, v20
	v_mul_f32_e32 v14, v14, v20
	v_fma_f32 v6, v106, v6, v110
	v_fma_f32 v14, v82, v14, v90
	v_mul_f32_e32 v6, 0xbfb8aa3b, v6
	v_mul_f32_e32 v14, 0xbfb8aa3b, v14
	v_exp_f32_e32 v6, v6
	v_exp_f32_e32 v14, v14
	v_add_f32_e32 v2, 1.0, v2
	v_mul_f32_e32 v10, v10, v20
	v_rcp_f32_e32 v2, v2
	v_fma_f32 v10, v86, v10, v98
	v_mul_f32_e32 v10, 0xbfb8aa3b, v10
	v_exp_f32_e32 v10, v10
	v_add_f32_e32 v6, 1.0, v6
	v_add_f32_e32 v14, 1.0, v14
	v_rcp_f32_e32 v6, v6
	v_rcp_f32_e32 v22, v14
	v_mul_f32_e32 v14, v14, v2
	v_mul_f32_e32 v2, v7, v20
	v_mul_f32_e32 v3, v3, v20
	v_fma_f32 v2, v107, v2, v111
	v_fma_f32 v3, v95, v3, v103
	v_mul_f32_e32 v2, 0xbfb8aa3b, v2
	v_mul_f32_e32 v3, 0xbfb8aa3b, v3
	v_add_f32_e32 v10, 1.0, v10
	v_exp_f32_e32 v2, v2
	v_exp_f32_e32 v3, v3
	v_rcp_f32_e32 v21, v10
	v_mul_f32_e32 v10, v10, v6
	v_mul_f32_e32 v6, v11, v20
	v_mul_f32_e32 v7, v15, v20
	v_fma_f32 v6, v87, v6, v99
	v_fma_f32 v7, v83, v7, v91
	v_mul_f32_e32 v6, 0xbfb8aa3b, v6
	v_mul_f32_e32 v7, 0xbfb8aa3b, v7
	v_exp_f32_e32 v6, v6
	v_exp_f32_e32 v7, v7
	v_add_f32_e32 v2, 1.0, v2
	v_add_f32_e32 v3, 1.0, v3
	v_rcp_f32_e32 v2, v2
	v_rcp_f32_e32 v3, v3
	v_add_f32_e32 v6, 1.0, v6
	v_add_f32_e32 v7, 1.0, v7
	v_mul_f32_e32 v23, v6, v2
	v_mul_f32_e32 v24, v7, v3
	v_mul_f32_e32 v2, v8, v20
	v_mul_f32_e32 v3, v4, v20
	v_fma_f32 v2, v108, v2, v112
	v_fma_f32 v3, v96, v3, v104
	v_mul_f32_e32 v2, 0xbfb8aa3b, v2
	v_mul_f32_e32 v3, 0xbfb8aa3b, v3
	v_exp_f32_e32 v2, v2
	v_exp_f32_e32 v3, v3
	v_rcp_f32_e32 v11, v6
	v_mul_f32_e32 v4, v12, v20
	v_mul_f32_e32 v6, v16, v20
	v_fma_f32 v4, v88, v4, v100
	v_fma_f32 v6, v84, v6, v92
	v_mul_f32_e32 v4, 0xbfb8aa3b, v4
	v_mul_f32_e32 v6, 0xbfb8aa3b, v6
	v_exp_f32_e32 v4, v4
	v_exp_f32_e32 v6, v6
	v_add_f32_e32 v2, 1.0, v2
	v_add_f32_e32 v3, 1.0, v3
	v_rcp_f32_e32 v2, v2
	v_rcp_f32_e32 v3, v3
	v_add_f32_e32 v4, 1.0, v4
	v_add_f32_e32 v6, 1.0, v6
	v_mul_f32_e32 v12, v4, v2
	v_mul_f32_e32 v16, v6, v3
	v_mul_f32_e32 v2, v9, v20
	v_mul_f32_e32 v3, v5, v20
	v_fmac_f32_e32 v113, v109, v2
	v_fmac_f32_e32 v105, v97, v3
	v_mul_f32_e32 v2, 0xbfb8aa3b, v113
	v_mul_f32_e32 v3, 0xbfb8aa3b, v105
	v_rcp_f32_e32 v15, v7
	v_rcp_f32_e32 v7, v4
	v_exp_f32_e32 v2, v2
	v_exp_f32_e32 v3, v3
	v_mul_f32_e32 v4, v13, v20
	v_fmac_f32_e32 v101, v89, v4
	v_mul_f32_e32 v5, v17, v20
	v_mul_f32_e32 v4, 0xbfb8aa3b, v101
	v_fmac_f32_e32 v93, v85, v5
	v_exp_f32_e32 v4, v4
	v_mul_f32_e32 v5, 0xbfb8aa3b, v93
	v_exp_f32_e32 v5, v5
	v_add_f32_e32 v2, 1.0, v2
	v_add_f32_e32 v3, 1.0, v3
	v_rcp_f32_e32 v2, v2
	v_rcp_f32_e32 v3, v3
	v_add_f32_e32 v4, 1.0, v4
	v_rcp_f32_e32 v8, v6
	v_add_f32_e32 v5, 1.0, v5
	v_rcp_f32_e32 v6, v4
	v_rcp_f32_e32 v9, v5
	v_mul_f32_e32 v13, v4, v2
	v_mul_f32_e32 v17, v5, v3
	v_cvt_pk_bf16_f32 v2, v21, v11
	v_cvt_pk_bf16_f32 v3, v7, v6
	v_lshlrev_b64 v[6:7], 12, v[18:19]
	v_cvt_pk_bf16_f32 v4, v22, v15
	v_cvt_pk_bf16_f32 v5, v8, v9
	v_lshl_add_u64 v[8:9], s[16:17], 0, v[6:7]
	v_lshl_add_u64 v[6:7], s[10:11], 0, v[6:7]
	v_lshl_add_u64 v[8:9], v[8:9], 0, v[146:147]
	v_lshl_add_u64 v[6:7], v[6:7], 0, v[146:147]
	global_store_dwordx4 v[8:9], v[2:5], off
	s_nop 1
	v_cvt_pk_bf16_f32 v2, v10, v23
	v_cvt_pk_bf16_f32 v3, v12, v13
	v_cvt_pk_bf16_f32 v4, v14, v24
	v_cvt_pk_bf16_f32 v5, v16, v17
	global_store_dwordx4 v[6:7], v[2:5], off
	s_cbranch_vccnz .LBB0_872
	s_andn2_b64 vcc, exec, s[8:9]
	s_cbranch_vccnz .LBB0_871
	s_barrier
	s_branch .LBB0_871

.LBB0_1301:
	s_nop 0
	s_or_b64 exec, exec, s[6:7]
	v_cmp_gt_i32_e64 s[6:7], 32, v6
	s_and_saveexec_b64 s[8:9], s[6:7]
	v_lshl_add_u32 v2, v6, 2, 0
	v_add_u32_e32 v2, 0x1fd00, v2
	v_mov_b32_e32 v3, 0
	ds_write_b32 v2, v3
	s_or_b64 exec, exec, s[8:9]
	v_readlane_b32 s2, v255, 9
	v_readlane_b32 s3, v255, 10
	s_waitcnt lgkmcnt(0)
	s_barrier
	s_load_dword s2, s[2:3], 0x98
	s_waitcnt lgkmcnt(0)
	s_cmp_lg_u32 s2, 0
	s_cselect_b64 s[12:13], -1, 0
	s_cmpk_gt_i32 s94, 0xff
	s_cselect_b64 s[8:9], -1, 0
	s_or_b64 s[8:9], s[8:9], s[12:13]
	s_and_b64 vcc, exec, s[8:9]
	s_cbranch_vccnz .LBB0_1316
	s_movk_i32 s2, 0x100
	v_cmp_gt_i32_e32 vcc, s2, v6
	v_lshlrev_b32_e32 v4, 2, v6
	s_add_i32 s2, 0, 0x1fd00
	v_add_u32_e32 v7, s2, v4
	v_lshlrev_b32_e32 v2, 6, v6
	s_add_i32 s2, 0, 0x1fd80
	v_ashrrev_i32_e32 v3, 31, v2
	v_add_u32_e32 v8, s2, v4
	s_lshl_b32 s2, s94, 8
	v_lshl_add_u64 v[2:3], v[2:3], 2, s[26:27]
	s_mov_b64 s[8:9], 0x4a000
	s_add_i32 s2, s86, s2
	s_lshl_b32 s3, s94, 7
	v_lshl_add_u64 v[2:3], v[2:3], 0, s[8:9]
	v_ashrrev_i32_e32 v9, 1, v6
	s_lshl_b32 s18, s28, 7
	v_add_u32_e32 v4, s2, v1
	s_lshl_b32 s19, s28, 8
	v_mov_b32_e32 v10, 1
	v_mov_b32_e32 v11, 0
	s_branch .LBB0_1306

.LBB0_1386:
	s_nop 0
	s_or_b64 exec, exec, s[6:7]
	s_add_i32 s2, 0, 0x200c0
	v_mov_b32_e32 v1, s2
	s_waitcnt lgkmcnt(0)
	s_barrier
	ds_read_b32 v1, v1
	s_ashr_i32 s29, s28, 31
	s_waitcnt lgkmcnt(0)
	v_readfirstlane_b32 s46, v1
	s_ashr_i32 s47, s46, 31
	s_lshl_b64 s[14:15], s[46:47], 2
	s_or_b64 s[6:7], s[14:15], s[28:29]
	s_mov_b32 s5, s7
	s_cmp_lg_u64 s[4:5], 0
	s_cbranch_scc0 .LBB0_1411
	s_ashr_i32 s4, s29, 31
	s_add_u32 s6, s28, s4
	s_mov_b32 s5, s4
	s_addc_u32 s7, s29, s4
	s_xor_b64 s[4:5], s[6:7], s[4:5]
	v_cvt_f32_u32_e32 v1, s4
	v_cvt_f32_u32_e32 v2, s5
	s_sub_u32 s2, 0, s4
	s_subb_u32 s3, 0, s5
	v_fmamk_f32 v1, v2, 0x4f800000, v1
	v_rcp_f32_e32 v1, v1
	s_nop 0
	v_mul_f32_e32 v1, 0x5f7ffffc, v1
	v_mul_f32_e32 v2, 0x2f800000, v1
	v_trunc_f32_e32 v2, v2
	v_fmamk_f32 v1, v2, 0xcf800000, v1
	v_cvt_u32_f32_e32 v2, v2
	v_cvt_u32_f32_e32 v1, v1
	v_readfirstlane_b32 s10, v2
	v_readfirstlane_b32 s8, v1
	s_mul_i32 s9, s2, s10
	s_mul_hi_u32 s12, s2, s8
	s_mul_i32 s11, s3, s8
	s_add_i32 s9, s12, s9
	s_add_i32 s9, s9, s11
	s_mul_i32 s13, s2, s8
	s_mul_i32 s12, s8, s9
	s_mul_hi_u32 s16, s8, s13
	s_mul_hi_u32 s11, s8, s9
	s_add_u32 s12, s16, s12
	s_addc_u32 s11, 0, s11
	s_mul_hi_u32 s17, s10, s13
	s_mul_i32 s13, s10, s13
	s_add_u32 s12, s12, s13
	s_mul_hi_u32 s16, s10, s9
	s_addc_u32 s11, s11, s17
	s_addc_u32 s12, s16, 0
	s_mul_i32 s9, s10, s9
	s_add_u32 s9, s11, s9
	s_addc_u32 s11, 0, s12
	s_add_u32 s12, s8, s9
	s_cselect_b64 s[8:9], -1, 0
	s_cmp_lg_u64 s[8:9], 0
	s_addc_u32 s10, s10, s11
	s_mul_i32 s8, s2, s10
	s_mul_hi_u32 s9, s2, s12
	s_add_i32 s8, s9, s8
	s_mul_i32 s3, s3, s12
	s_add_i32 s8, s8, s3
	s_mul_i32 s2, s2, s12
	s_mul_hi_u32 s9, s10, s2
	s_mul_i32 s11, s10, s2
	s_mul_i32 s16, s12, s8
	s_mul_hi_u32 s2, s12, s2
	s_mul_hi_u32 s13, s12, s8
	s_add_u32 s2, s2, s16
	s_addc_u32 s13, 0, s13
	s_add_u32 s2, s2, s11
	s_mul_hi_u32 s3, s10, s8
	s_addc_u32 s2, s13, s9
	s_addc_u32 s3, s3, 0
	s_mul_i32 s8, s10, s8
	s_add_u32 s2, s2, s8
	s_addc_u32 s3, 0, s3
	s_add_u32 s2, s12, s2
	s_cselect_b64 s[8:9], -1, 0
	s_cmp_lg_u64 s[8:9], 0
	s_addc_u32 s3, s10, s3
	s_ashr_i32 s8, s15, 31
	s_add_u32 s10, s14, s8
	s_mov_b32 s9, s8
	s_addc_u32 s11, s15, s8
	s_xor_b64 s[10:11], s[10:11], s[8:9]
	s_mul_i32 s13, s10, s3
	s_mul_hi_u32 s16, s10, s2
	s_mul_hi_u32 s12, s10, s3
	s_add_u32 s13, s16, s13
	s_addc_u32 s12, 0, s12
	s_mul_hi_u32 s17, s11, s2
	s_mul_i32 s2, s11, s2
	s_add_u32 s2, s13, s2
	s_mul_hi_u32 s16, s11, s3
	s_addc_u32 s2, s12, s17
	s_addc_u32 s12, s16, 0
	s_mul_i32 s3, s11, s3
	s_add_u32 s2, s2, s3
	s_addc_u32 s3, 0, s12
	s_mul_i32 s3, s4, s3
	s_mul_hi_u32 s12, s4, s2
	s_add_i32 s3, s12, s3
	s_mul_i32 s12, s5, s2
	s_add_i32 s3, s3, s12
	s_sub_i32 s16, s11, s3
	s_mul_i32 s2, s4, s2
	s_sub_u32 s2, s10, s2
	s_cselect_b64 s[12:13], -1, 0
	s_cmp_lg_u64 s[12:13], 0
	s_subb_u32 s10, s16, s5
	s_sub_u32 s22, s2, s4
	s_cselect_b64 s[16:17], -1, 0
	s_cmp_lg_u64 s[16:17], 0
	s_subb_u32 s23, s10, 0
	s_cmp_ge_u32 s23, s5
	s_cselect_b32 s24, -1, 0
	s_cmp_ge_u32 s22, s4
	s_cselect_b32 s25, -1, 0
	s_cmp_eq_u32 s23, s5
	s_cselect_b32 s24, s25, s24
	s_cmp_lg_u64 s[16:17], 0
	s_subb_u32 s10, s10, s5
	s_sub_u32 s25, s22, s4
	s_cselect_b64 s[16:17], -1, 0
	s_cmp_lg_u64 s[16:17], 0
	s_subb_u32 s10, s10, 0
	s_cmp_lg_u32 s24, 0
	s_cselect_b32 s16, s25, s22
	s_cselect_b32 s10, s10, s23
	s_cmp_lg_u64 s[12:13], 0
	s_subb_u32 s3, s11, s3
	s_cmp_ge_u32 s3, s5
	s_cselect_b32 s11, -1, 0
	s_cmp_ge_u32 s2, s4
	s_cselect_b32 s4, -1, 0
	s_cmp_eq_u32 s3, s5
	s_cselect_b32 s4, s4, s11
	s_cmp_lg_u32 s4, 0
	s_cselect_b32 s5, s10, s3
	s_cselect_b32 s4, s16, s2
	s_xor_b64 s[4:5], s[4:5], s[8:9]
	s_sub_u32 s4, s4, s8
	s_subb_u32 s5, s5, s8
	s_cbranch_execnz .LBB0_1389
